# K-loop: s_setprio 1 issued before the barrier that opens each MFMA segment (the wave holds the raise at release), on top of one raise per segment
# baseline (speedup 1.0000x reference)
; #define PG8_STAGE(bufoff, gbase, voff) do { _Pragma("unroll") for (int _i = 0; _i < 2; ++_i) \
;         __builtin_amdgcn_global_load_lds((const unsigned*)((const char*)(gbase) + (voff)[_i]), (PG8_LAS unsigned*)(lds + (bufoff) + ldsw + _i * 8192), 16, 0, 0); } while (0)
; #define PG8_LDA(dst, b, h) do { _Pragma("unroll") for (int m = 0; m < 4; ++m) { const bf16x8 f0_ = *(const PG8_LAS bf16x8*)(lds + PG8_SA(b, h) + aoff + m * 2048), f1_ = *(const PG8_LAS bf16x8*)(lds + PG8_SA(b, h) + aoff + m * 2048 + 1024); dst[m].set(f0_, f1_); } } while (0)
; #define PG8_LDB(dst, b, h) do { _Pragma("unroll") for (int n = 0; n < 2; ++n) { const bf16x8 f0_ = *(const PG8_LAS bf16x8*)(lds + PG8_SB(b, h) + boff + n * 2048), f1_ = *(const PG8_LAS bf16x8*)(lds + PG8_SB(b, h) + boff + n * 2048 + 1024); dst[n].set(f0_, f1_); } } while (0)
; #define PG8_WAIT_V(n) asm volatile("s_waitcnt vmcnt(" #n ")" ::: "memory")
; #define PG8_WAIT_L(n) asm volatile("s_waitcnt lgkmcnt(" #n ")" ::: "memory")
; #define PG8_BAR __builtin_amdgcn_s_barrier()
; #define PG8_SCHED __builtin_amdgcn_sched_barrier(0)
; template <class Epi, class Sched, bool ALIGN_EPI = false, bool SP2 = false>
; __device__ __forceinline__ void gemm_phase(PG8_LAS unsigned char* lds, const Gemm g, const Sched& S, const Epi& E) {
;     ...
;             PG8_LDB(B0, 0, 0); PG8_LDB(B1, 0, 1); PG8_SCHED; PG8_LDA(At, 0, 0); PG8_STAGE(PG8_SA(1, 1), a1 + hstep, voffA);
;             PG8_WAIT_V(8); PG8_WAIT_L(0); PG8_BAR; PG8_MMA(0, 0, At, B0); PG8_MMA(0, 1, At, B1); PG8_BAR; PG8_SCHED;
;             PG8_LDA(At, 0, 1); PG8_STAGE(PG8_SB(0, 0), b2, voffB); PG8_STAGE(PG8_SB(0, 1), b2 + hstepB, voffB); PG8_STAGE(PG8_SA(0, 0), a2, voffA);
;             PG8_WAIT_V(8); PG8_WAIT_L(0); PG8_BAR; PG8_MMA(1, 0, At, B0); PG8_MMA(1, 1, At, B1); PG8_BAR; PG8_SCHED;
.Lkr0_a:
	v_lshl_add_u64 v[190:191], s[2:3], 0, v[174:175]
	s_add_i32 m0, s58, 0xc000
	ds_read_b128 v[182:185], v205
	ds_read_b128 v[186:189], v205 offset:1024
	ds_read_b128 v[212:215], v205 offset:2048
	ds_read_b128 v[216:219], v205 offset:3072
	ds_read_b128 v[220:223], v205 offset:4096
	ds_read_b128 v[224:227], v205 offset:5120
	ds_read_b128 v[228:231], v205 offset:6144
	ds_read_b128 v[232:235], v205 offset:7168
	global_load_lds_dwordx4 v[190:191], off
	v_lshl_add_u64 v[190:191], s[2:3], 0, v[176:177]
	s_add_i32 m0, s58, 0xe000
	s_nop 0
	global_load_lds_dwordx4 v[190:191], off
	s_waitcnt vmcnt(8)
	s_waitcnt lgkmcnt(0)
	s_setprio 1
	s_barrier
	s_waitcnt lgkmcnt(0)
	v_mfma_scale_f32_16x16x128_f8f6f4 v[158:161], v[18:25], v[182:189], v[158:161], v206, v207 op_sel_hi:[0,0,0]
	v_mfma_scale_f32_16x16x128_f8f6f4 v[154:157], v[26:33], v[182:189], v[154:157], v206, v207 op_sel_hi:[0,0,0]
	v_mfma_scale_f32_16x16x128_f8f6f4 v[142:145], v[18:25], v[212:219], v[142:145], v206, v207 op_sel_hi:[0,0,0]
	v_mfma_scale_f32_16x16x128_f8f6f4 v[138:141], v[26:33], v[212:219], v[138:141], v206, v207 op_sel_hi:[0,0,0]
	v_mfma_scale_f32_16x16x128_f8f6f4 v[126:129], v[18:25], v[220:227], v[126:129], v206, v207 op_sel_hi:[0,0,0]
	v_mfma_scale_f32_16x16x128_f8f6f4 v[122:125], v[26:33], v[220:227], v[122:125], v206, v207 op_sel_hi:[0,0,0]
	v_mfma_scale_f32_16x16x128_f8f6f4 v[110:113], v[18:25], v[228:235], v[110:113], v206, v207 op_sel_hi:[0,0,0]
	v_mfma_scale_f32_16x16x128_f8f6f4 v[106:109], v[26:33], v[228:235], v[106:109], v206, v207 op_sel_hi:[0,0,0]
	v_mfma_scale_f32_16x16x128_f8f6f4 v[150:153], v[2:9], v[182:189], v[150:153], v206, v207 op_sel_hi:[0,0,0]
	v_mfma_scale_f32_16x16x128_f8f6f4 v[146:149], v[10:17], v[182:189], v[146:149], v206, v207 op_sel_hi:[0,0,0]
	v_mfma_scale_f32_16x16x128_f8f6f4 v[134:137], v[2:9], v[212:219], v[134:137], v206, v207 op_sel_hi:[0,0,0]
	v_mfma_scale_f32_16x16x128_f8f6f4 v[130:133], v[10:17], v[212:219], v[130:133], v206, v207 op_sel_hi:[0,0,0]
	v_mfma_scale_f32_16x16x128_f8f6f4 v[118:121], v[2:9], v[220:227], v[118:121], v206, v207 op_sel_hi:[0,0,0]
	v_mfma_scale_f32_16x16x128_f8f6f4 v[114:117], v[10:17], v[220:227], v[114:117], v206, v207 op_sel_hi:[0,0,0]
	v_mfma_scale_f32_16x16x128_f8f6f4 v[102:105], v[2:9], v[228:235], v[102:105], v206, v207 op_sel_hi:[0,0,0]
	v_mfma_scale_f32_16x16x128_f8f6f4 v[98:101], v[10:17], v[228:235], v[98:101], v206, v207 op_sel_hi:[0,0,0]
	s_setprio 0
	s_barrier
	s_add_i32 s0, s76, s57
	v_lshl_add_u64 v[182:183], s[50:51], 0, v[164:165]
	s_mov_b32 m0, s0
	ds_read_b128 v[212:215], v205 offset:16384
	ds_read_b128 v[216:219], v205 offset:17408
	ds_read_b128 v[220:223], v205 offset:18432
	ds_read_b128 v[224:227], v205 offset:19456
	ds_read_b128 v[228:231], v205 offset:20480
	ds_read_b128 v[232:235], v205 offset:21504
	ds_read_b128 v[236:239], v205 offset:22528
	ds_read_b128 v[240:243], v205 offset:23552
	global_load_lds_dwordx4 v[182:183], off
	s_add_i32 m0, s0, 0x2000
	v_lshl_add_u64 v[184:185], s[50:51], 0, v[168:169]
	s_add_u32 s50, s50, s16
	s_addc_u32 s51, s51, s17
	s_add_i32 s0, s77, s57
	global_load_lds_dwordx4 v[184:185], off
	v_lshl_add_u64 v[186:187], s[50:51], 0, v[164:165]
	s_mov_b32 m0, s0
	v_lshl_add_u64 v[188:189], s[50:51], 0, v[168:169]
	global_load_lds_dwordx4 v[186:187], off
	s_add_i32 m0, s0, 0x2000
	v_lshl_add_u64 v[190:191], s[48:49], 0, v[162:163]
	global_load_lds_dwordx4 v[188:189], off
	v_lshl_add_u64 v[192:193], s[48:49], 0, v[166:167]
	s_waitcnt vmcnt(6)
	s_waitcnt lgkmcnt(0)
	s_setprio 1
	s_barrier
	s_waitcnt lgkmcnt(0)
	v_mfma_scale_f32_16x16x128_f8f6f4 v[94:97], v[18:25], v[212:219], v[94:97], v206, v207 op_sel_hi:[0,0,0]
	v_mfma_scale_f32_16x16x128_f8f6f4 v[90:93], v[26:33], v[212:219], v[90:93], v206, v207 op_sel_hi:[0,0,0]
	v_mfma_scale_f32_16x16x128_f8f6f4 v[78:81], v[18:25], v[220:227], v[78:81], v206, v207 op_sel_hi:[0,0,0]
	v_mfma_scale_f32_16x16x128_f8f6f4 v[74:77], v[26:33], v[220:227], v[74:77], v206, v207 op_sel_hi:[0,0,0]
	v_mfma_scale_f32_16x16x128_f8f6f4 v[62:65], v[18:25], v[228:235], v[62:65], v206, v207 op_sel_hi:[0,0,0]
	v_mfma_scale_f32_16x16x128_f8f6f4 v[58:61], v[26:33], v[228:235], v[58:61], v206, v207 op_sel_hi:[0,0,0]
	v_mfma_scale_f32_16x16x128_f8f6f4 v[46:49], v[18:25], v[236:243], v[46:49], v206, v207 op_sel_hi:[0,0,0]
	v_mfma_scale_f32_16x16x128_f8f6f4 v[42:45], v[26:33], v[236:243], v[42:45], v206, v207 op_sel_hi:[0,0,0]
	v_mfma_scale_f32_16x16x128_f8f6f4 v[86:89], v[2:9], v[212:219], v[86:89], v206, v207 op_sel_hi:[0,0,0]
	v_mfma_scale_f32_16x16x128_f8f6f4 v[82:85], v[10:17], v[212:219], v[82:85], v206, v207 op_sel_hi:[0,0,0]
	v_mfma_scale_f32_16x16x128_f8f6f4 v[70:73], v[2:9], v[220:227], v[70:73], v206, v207 op_sel_hi:[0,0,0]
	v_mfma_scale_f32_16x16x128_f8f6f4 v[66:69], v[10:17], v[220:227], v[66:69], v206, v207 op_sel_hi:[0,0,0]
	v_mfma_scale_f32_16x16x128_f8f6f4 v[54:57], v[2:9], v[228:235], v[54:57], v206, v207 op_sel_hi:[0,0,0]
	v_mfma_scale_f32_16x16x128_f8f6f4 v[50:53], v[10:17], v[228:235], v[50:53], v206, v207 op_sel_hi:[0,0,0]
	v_mfma_scale_f32_16x16x128_f8f6f4 v[38:41], v[2:9], v[236:243], v[38:41], v206, v207 op_sel_hi:[0,0,0]
	v_mfma_scale_f32_16x16x128_f8f6f4 v[34:37], v[10:17], v[236:243], v[34:37], v206, v207 op_sel_hi:[0,0,0]
	s_setprio 0
	s_barrier
; #define PG8_STAGE(bufoff, gbase, voff) do { _Pragma("unroll") for (int _i = 0; _i < 2; ++_i) \
;         __builtin_amdgcn_global_load_lds((const unsigned*)((const char*)(gbase) + (voff)[_i]), (PG8_LAS unsigned*)(lds + (bufoff) + ldsw + _i * 8192), 16, 0, 0); } while (0)
; #define PG8_LDA(dst, b, h) do { _Pragma("unroll") for (int m = 0; m < 4; ++m) { const bf16x8 f0_ = *(const PG8_LAS bf16x8*)(lds + PG8_SA(b, h) + aoff + m * 2048), f1_ = *(const PG8_LAS bf16x8*)(lds + PG8_SA(b, h) + aoff + m * 2048 + 1024); dst[m].set(f0_, f1_); } } while (0)
; #define PG8_LDB(dst, b, h) do { _Pragma("unroll") for (int n = 0; n < 2; ++n) { const bf16x8 f0_ = *(const PG8_LAS bf16x8*)(lds + PG8_SB(b, h) + boff + n * 2048), f1_ = *(const PG8_LAS bf16x8*)(lds + PG8_SB(b, h) + boff + n * 2048 + 1024); dst[n].set(f0_, f1_); } } while (0)
; #define PG8_WAIT_V(n) asm volatile("s_waitcnt vmcnt(" #n ")" ::: "memory")
; #define PG8_WAIT_L(n) asm volatile("s_waitcnt lgkmcnt(" #n ")" ::: "memory")
; #define PG8_BAR __builtin_amdgcn_s_barrier()
; #define PG8_SCHED __builtin_amdgcn_sched_barrier(0)
; template <class Epi, class Sched, bool ALIGN_EPI = false, bool SP2 = false>
; __device__ __forceinline__ void gemm_phase(PG8_LAS unsigned char* lds, const Gemm g, const Sched& S, const Epi& E) {
;     ...
;             PG8_WAIT_V(8); PG8_WAIT_L(0); PG8_BAR; PG8_MMA(1, 0, At, B0); PG8_MMA(1, 1, At, B1); PG8_BAR; PG8_SCHED;
;             PG8_LDB(B0, 1, 0); PG8_LDB(B1, 1, 1); PG8_SCHED; PG8_LDA(At, 1, 0); PG8_STAGE(PG8_SA(0, 1), a2 + hstep, voffA);
;             PG8_WAIT_V(8); PG8_WAIT_L(0); PG8_BAR; PG8_MMA(0, 0, At, B0); PG8_MMA(0, 1, At, B1); PG8_BAR; PG8_SCHED;
;             PG8_LDA(At, 1, 1); PG8_STAGE(PG8_SB(1, 0), b3, voffB); PG8_STAGE(PG8_SB(1, 1), b3 + hstepB, voffB); PG8_STAGE(PG8_SA(1, 0), a3, voffA);
;             PG8_WAIT_V(8); PG8_WAIT_L(0); PG8_BAR; PG8_MMA(1, 0, At, B0); PG8_MMA(1, 1, At, B1); PG8_BAR; PG8_SCHED;
	s_add_i32 s0, 0, 0x18000
	s_add_i32 s1, 0, 0x1c000
	v_add_u32_e32 v14, s0, v194
	v_add_u32_e32 v30, s1, v194
	ds_read_b128 v[2:5], v14
	ds_read_b128 v[6:9], v14 offset:1024
	ds_read_b128 v[10:13], v14 offset:2048
	ds_read_b128 v[14:17], v14 offset:3072
	ds_read_b128 v[18:21], v30
	ds_read_b128 v[22:25], v30 offset:1024
	ds_read_b128 v[26:29], v30 offset:2048
	ds_read_b128 v[30:33], v30 offset:3072
	s_add_u32 s48, s48, s14
	s_addc_u32 s49, s49, s15
	s_mov_b32 m0, s61
	v_lshl_add_u64 v[244:245], s[48:49], 0, v[162:163]
	ds_read_b128 v[212:215], v205 offset:32768
	ds_read_b128 v[216:219], v205 offset:33792
	ds_read_b128 v[220:223], v205 offset:34816
	ds_read_b128 v[224:227], v205 offset:35840
	ds_read_b128 v[228:231], v205 offset:36864
	ds_read_b128 v[232:235], v205 offset:37888
	ds_read_b128 v[236:239], v205 offset:38912
	ds_read_b128 v[240:243], v205 offset:39936
	s_mov_b32 m0, s58
	s_nop 0
	global_load_lds_dwordx4 v[190:191], off
	s_mov_b32 m0, s59
	s_nop 0
	global_load_lds_dwordx4 v[192:193], off
	s_mov_b32 m0, s61
	s_nop 0
	global_load_lds_dwordx4 v[244:245], off
	v_lshl_add_u64 v[244:245], s[48:49], 0, v[166:167]
	s_mov_b32 m0, s63
	s_nop 0
	global_load_lds_dwordx4 v[244:245], off
	s_waitcnt vmcnt(8)
	s_waitcnt lgkmcnt(0)
	s_setprio 1
	s_barrier
	s_waitcnt lgkmcnt(0)
	v_mfma_scale_f32_16x16x128_f8f6f4 v[158:161], v[2:9], v[212:219], v[158:161], v206, v207 op_sel_hi:[0,0,0]
	v_mfma_scale_f32_16x16x128_f8f6f4 v[154:157], v[10:17], v[212:219], v[154:157], v206, v207 op_sel_hi:[0,0,0]
	v_mfma_scale_f32_16x16x128_f8f6f4 v[142:145], v[2:9], v[220:227], v[142:145], v206, v207 op_sel_hi:[0,0,0]
	v_mfma_scale_f32_16x16x128_f8f6f4 v[138:141], v[10:17], v[220:227], v[138:141], v206, v207 op_sel_hi:[0,0,0]
	v_mfma_scale_f32_16x16x128_f8f6f4 v[126:129], v[2:9], v[228:235], v[126:129], v206, v207 op_sel_hi:[0,0,0]
	v_mfma_scale_f32_16x16x128_f8f6f4 v[122:125], v[10:17], v[228:235], v[122:125], v206, v207 op_sel_hi:[0,0,0]
	v_mfma_scale_f32_16x16x128_f8f6f4 v[110:113], v[2:9], v[236:243], v[110:113], v206, v207 op_sel_hi:[0,0,0]
	v_mfma_scale_f32_16x16x128_f8f6f4 v[106:109], v[10:17], v[236:243], v[106:109], v206, v207 op_sel_hi:[0,0,0]
	v_mfma_scale_f32_16x16x128_f8f6f4 v[150:153], v[18:25], v[212:219], v[150:153], v206, v207 op_sel_hi:[0,0,0]
	v_mfma_scale_f32_16x16x128_f8f6f4 v[146:149], v[26:33], v[212:219], v[146:149], v206, v207 op_sel_hi:[0,0,0]
	v_mfma_scale_f32_16x16x128_f8f6f4 v[134:137], v[18:25], v[220:227], v[134:137], v206, v207 op_sel_hi:[0,0,0]
	v_mfma_scale_f32_16x16x128_f8f6f4 v[130:133], v[26:33], v[220:227], v[130:133], v206, v207 op_sel_hi:[0,0,0]
	v_mfma_scale_f32_16x16x128_f8f6f4 v[118:121], v[18:25], v[228:235], v[118:121], v206, v207 op_sel_hi:[0,0,0]
	v_mfma_scale_f32_16x16x128_f8f6f4 v[114:117], v[26:33], v[228:235], v[114:117], v206, v207 op_sel_hi:[0,0,0]
	v_mfma_scale_f32_16x16x128_f8f6f4 v[102:105], v[18:25], v[236:243], v[102:105], v206, v207 op_sel_hi:[0,0,0]
	v_mfma_scale_f32_16x16x128_f8f6f4 v[98:101], v[26:33], v[236:243], v[98:101], v206, v207 op_sel_hi:[0,0,0]
	s_setprio 0
	s_barrier
	s_add_i32 s0, s0, s57
	v_lshl_add_u64 v[182:183], v[182:183], 0, s[36:37]
	s_mov_b32 m0, s0
	ds_read_b128 v[212:215], v205 offset:49152
	ds_read_b128 v[216:219], v205 offset:50176
	ds_read_b128 v[220:223], v205 offset:51200
	ds_read_b128 v[224:227], v205 offset:52224
	ds_read_b128 v[228:231], v205 offset:53248
	ds_read_b128 v[232:235], v205 offset:54272
	ds_read_b128 v[236:239], v205 offset:55296
	ds_read_b128 v[240:243], v205 offset:56320
	global_load_lds_dwordx4 v[182:183], off
	v_lshl_add_u64 v[182:183], v[184:185], 0, s[36:37]
	s_add_i32 m0, s0, 0x2000
	s_add_i32 s0, s1, s57
	global_load_lds_dwordx4 v[182:183], off
	v_lshl_add_u64 v[182:183], v[186:187], 0, s[36:37]
	s_mov_b32 m0, s0
	s_nop 0
	global_load_lds_dwordx4 v[182:183], off
	v_lshl_add_u64 v[182:183], v[188:189], 0, s[36:37]
	s_add_i32 m0, s0, 0x2000
	s_nop 0
	global_load_lds_dwordx4 v[182:183], off
	s_cmp_ge_i32 s53, s69
	s_cbranch_scc0 .Lkr0_b
	v_lshl_add_u64 v[182:183], v[190:191], 0, s[36:37]
	s_mov_b32 m0, s66
	s_nop 0
	global_load_lds_dwordx4 v[182:183], off
	v_lshl_add_u64 v[182:183], v[192:193], 0, s[36:37]
	s_mov_b32 m0, s67
	s_nop 0
	global_load_lds_dwordx4 v[182:183], off
.Lkr0_b:
	s_waitcnt vmcnt(6)
	s_waitcnt lgkmcnt(0)
	s_setprio 1
	s_barrier
	s_waitcnt lgkmcnt(0)
	v_mfma_scale_f32_16x16x128_f8f6f4 v[94:97], v[2:9], v[212:219], v[94:97], v206, v207 op_sel_hi:[0,0,0]
	v_mfma_scale_f32_16x16x128_f8f6f4 v[90:93], v[10:17], v[212:219], v[90:93], v206, v207 op_sel_hi:[0,0,0]
	v_mfma_scale_f32_16x16x128_f8f6f4 v[78:81], v[2:9], v[220:227], v[78:81], v206, v207 op_sel_hi:[0,0,0]
	v_mfma_scale_f32_16x16x128_f8f6f4 v[74:77], v[10:17], v[220:227], v[74:77], v206, v207 op_sel_hi:[0,0,0]
	v_mfma_scale_f32_16x16x128_f8f6f4 v[62:65], v[2:9], v[228:235], v[62:65], v206, v207 op_sel_hi:[0,0,0]
	v_mfma_scale_f32_16x16x128_f8f6f4 v[58:61], v[10:17], v[228:235], v[58:61], v206, v207 op_sel_hi:[0,0,0]
	v_mfma_scale_f32_16x16x128_f8f6f4 v[46:49], v[2:9], v[236:243], v[46:49], v206, v207 op_sel_hi:[0,0,0]
	v_mfma_scale_f32_16x16x128_f8f6f4 v[42:45], v[10:17], v[236:243], v[42:45], v206, v207 op_sel_hi:[0,0,0]
	v_mfma_scale_f32_16x16x128_f8f6f4 v[86:89], v[18:25], v[212:219], v[86:89], v206, v207 op_sel_hi:[0,0,0]
	v_mfma_scale_f32_16x16x128_f8f6f4 v[82:85], v[26:33], v[212:219], v[82:85], v206, v207 op_sel_hi:[0,0,0]
	v_mfma_scale_f32_16x16x128_f8f6f4 v[70:73], v[18:25], v[220:227], v[70:73], v206, v207 op_sel_hi:[0,0,0]
	v_mfma_scale_f32_16x16x128_f8f6f4 v[66:69], v[26:33], v[220:227], v[66:69], v206, v207 op_sel_hi:[0,0,0]
	v_mfma_scale_f32_16x16x128_f8f6f4 v[54:57], v[18:25], v[228:235], v[54:57], v206, v207 op_sel_hi:[0,0,0]
	v_mfma_scale_f32_16x16x128_f8f6f4 v[50:53], v[26:33], v[228:235], v[50:53], v206, v207 op_sel_hi:[0,0,0]
	v_mfma_scale_f32_16x16x128_f8f6f4 v[38:41], v[18:25], v[236:243], v[38:41], v206, v207 op_sel_hi:[0,0,0]
	v_mfma_scale_f32_16x16x128_f8f6f4 v[34:37], v[26:33], v[236:243], v[34:37], v206, v207 op_sel_hi:[0,0,0]
	s_setprio 0
	s_barrier
	s_add_u32 s2, s2, 0x100
	s_addc_u32 s3, s3, 0
	s_add_u32 s20, s20, 0x100
	s_addc_u32 s52, s52, 0
	s_cmp_ge_i32 s53, s69
	s_cselect_b32 s99, 0, 1
	s_mov_b32 s48, s53
	s_cbranch_scc0 .LBB0_204

; #define PG8_STAGE(bufoff, gbase, voff) do { _Pragma("unroll") for (int _i = 0; _i < 2; ++_i) \
;         __builtin_amdgcn_global_load_lds((const unsigned*)((const char*)(gbase) + (voff)[_i]), (PG8_LAS unsigned*)(lds + (bufoff) + ldsw + _i * 8192), 16, 0, 0); } while (0)
; #define PG8_LDA(dst, b, h) do { _Pragma("unroll") for (int m = 0; m < 4; ++m) { const bf16x8 f0_ = *(const PG8_LAS bf16x8*)(lds + PG8_SA(b, h) + aoff + m * 2048), f1_ = *(const PG8_LAS bf16x8*)(lds + PG8_SA(b, h) + aoff + m * 2048 + 1024); dst[m].set(f0_, f1_); } } while (0)
; #define PG8_LDB(dst, b, h) do { _Pragma("unroll") for (int n = 0; n < 2; ++n) { const bf16x8 f0_ = *(const PG8_LAS bf16x8*)(lds + PG8_SB(b, h) + boff + n * 2048), f1_ = *(const PG8_LAS bf16x8*)(lds + PG8_SB(b, h) + boff + n * 2048 + 1024); dst[n].set(f0_, f1_); } } while (0)
; #define PG8_WAIT_V(n) asm volatile("s_waitcnt vmcnt(" #n ")" ::: "memory")
; #define PG8_WAIT_L(n) asm volatile("s_waitcnt lgkmcnt(" #n ")" ::: "memory")
; #define PG8_BAR __builtin_amdgcn_s_barrier()
; #define PG8_SCHED __builtin_amdgcn_sched_barrier(0)
; template <class Epi, class Sched, bool ALIGN_EPI = false, bool SP2 = false>
; __device__ __forceinline__ void gemm_phase(PG8_LAS unsigned char* lds, const Gemm g, const Sched& S, const Epi& E) {
;     ...
;             const bool last = (t == nt - 2);
;             const char* a1 = cA + (size_t)(t + 1) * kstep;
;             const char* a2 = last ? nA : cA + (size_t)(t + 2) * kstep; const char* b2 = last ? nB : cB + (size_t)(t + 2) * kstep;
;             const char* a3 = a2 + kstep; const char* b3 = b2 + kstep;
;             if (last && has_next) S.a_ready(nxt);
;             if constexpr (SP2) {
;             PG8_LDB(B0, 0, 0); PG8_LDB(B1, 0, 1); PG8_SCHED; PG8_LDA(At, 0, 0); PG8_STAGE(PG8_SA(1, 1), a1 + hstep, voffA);
;             PG8_WAIT_V(8); PG8_WAIT_L(0); PG8_BAR; PG8_MMA(0, 0, At, B0); PG8_MMA(0, 1, At, B1); PG8_BAR; PG8_SCHED;
;             PG8_LDA(At, 0, 1); PG8_STAGE(PG8_SB(0, 0), b2, voffB); PG8_STAGE(PG8_SB(0, 1), b2 + hstepB, voffB); PG8_STAGE(PG8_SA(0, 0), a2, voffA);
;             PG8_WAIT_V(8); PG8_WAIT_L(0); PG8_BAR; PG8_MMA(1, 0, At, B0); PG8_MMA(1, 1, At, B1); PG8_BAR; PG8_SCHED;
.LBB0_984:
	s_add_i32 s75, s42, 2
	v_add_u32_e32 v186, s59, v173
	v_add_u32_e32 v202, s61, v173
	s_add_u32 s0, s38, s40
	ds_read_b128 v[168:171], v186
	ds_read_b128 v[178:181], v186 offset:1024
	ds_read_b128 v[182:185], v186 offset:2048
	ds_read_b128 v[186:189], v186 offset:3072
	ds_read_b128 v[190:193], v202
	ds_read_b128 v[194:197], v202 offset:1024
	ds_read_b128 v[198:201], v202 offset:2048
	ds_read_b128 v[202:205], v202 offset:3072
	s_addc_u32 s1, s39, s41
	s_add_u32 s0, s0, 0x100
	s_addc_u32 s1, s1, 0
	s_add_u32 s33, s73, s40
	s_addc_u32 s76, s74, s41
	s_cmp_eq_u32 s57, s42
	s_cselect_b32 s43, s3, s1
	s_cselect_b32 s42, s2, s0
	s_cselect_b32 s1, s37, s76
	s_cselect_b32 s0, s36, s33
	v_lshl_add_u64 v[240:241], v[164:165], 0, s[40:41]
	s_add_i32 m0, s47, 0xc000
	ds_read_b128 v[206:209], v176
	ds_read_b128 v[212:215], v176 offset:1024
	ds_read_b128 v[216:219], v176 offset:2048
	ds_read_b128 v[220:223], v176 offset:3072
	ds_read_b128 v[224:227], v176 offset:4096
	ds_read_b128 v[228:231], v176 offset:5120
	ds_read_b128 v[232:235], v176 offset:6144
	ds_read_b128 v[236:239], v176 offset:7168
	global_load_lds_dwordx4 v[240:241], off
	v_lshl_add_u64 v[240:241], v[166:167], 0, s[40:41]
	s_add_i32 m0, s47, 0xe000
	s_nop 0
	global_load_lds_dwordx4 v[240:241], off
	s_waitcnt vmcnt(8)
	s_waitcnt lgkmcnt(0)
	s_setprio 1
	s_barrier
	s_waitcnt lgkmcnt(0)
	v_mfma_f32_16x16x32_bf16 v[126:129], v[168:171], v[206:209], v[126:129]
	v_mfma_f32_16x16x32_bf16 v[122:125], v[182:185], v[206:209], v[122:125]
	v_mfma_f32_16x16x32_bf16 v[110:113], v[168:171], v[216:219], v[110:113]
	v_mfma_f32_16x16x32_bf16 v[106:109], v[182:185], v[216:219], v[106:109]
	v_mfma_f32_16x16x32_bf16 v[94:97], v[168:171], v[224:227], v[94:97]
	v_mfma_f32_16x16x32_bf16 v[90:93], v[182:185], v[224:227], v[90:93]
	v_mfma_f32_16x16x32_bf16 v[78:81], v[168:171], v[232:235], v[78:81]
	v_mfma_f32_16x16x32_bf16 v[74:77], v[182:185], v[232:235], v[74:77]
	v_mfma_f32_16x16x32_bf16 v[126:129], v[178:181], v[212:215], v[126:129]
	v_mfma_f32_16x16x32_bf16 v[122:125], v[186:189], v[212:215], v[122:125]
	v_mfma_f32_16x16x32_bf16 v[110:113], v[178:181], v[220:223], v[110:113]
	v_mfma_f32_16x16x32_bf16 v[106:109], v[186:189], v[220:223], v[106:109]
	v_mfma_f32_16x16x32_bf16 v[94:97], v[178:181], v[228:231], v[94:97]
	v_mfma_f32_16x16x32_bf16 v[90:93], v[186:189], v[228:231], v[90:93]
	v_mfma_f32_16x16x32_bf16 v[78:81], v[178:181], v[236:239], v[78:81]
	v_mfma_f32_16x16x32_bf16 v[74:77], v[186:189], v[236:239], v[74:77]
	v_mfma_f32_16x16x32_bf16 v[118:121], v[190:193], v[206:209], v[118:121]
	v_mfma_f32_16x16x32_bf16 v[114:117], v[198:201], v[206:209], v[114:117]
	v_mfma_f32_16x16x32_bf16 v[102:105], v[190:193], v[216:219], v[102:105]
	v_mfma_f32_16x16x32_bf16 v[98:101], v[198:201], v[216:219], v[98:101]
	v_mfma_f32_16x16x32_bf16 v[86:89], v[190:193], v[224:227], v[86:89]
	v_mfma_f32_16x16x32_bf16 v[82:85], v[198:201], v[224:227], v[82:85]
	v_mfma_f32_16x16x32_bf16 v[70:73], v[190:193], v[232:235], v[70:73]
	v_mfma_f32_16x16x32_bf16 v[66:69], v[198:201], v[232:235], v[66:69]
	v_mfma_f32_16x16x32_bf16 v[118:121], v[194:197], v[212:215], v[118:121]
	v_mfma_f32_16x16x32_bf16 v[114:117], v[202:205], v[212:215], v[114:117]
	v_mfma_f32_16x16x32_bf16 v[102:105], v[194:197], v[220:223], v[102:105]
	v_mfma_f32_16x16x32_bf16 v[98:101], v[202:205], v[220:223], v[98:101]
	v_mfma_f32_16x16x32_bf16 v[86:89], v[194:197], v[228:231], v[86:89]
	v_mfma_f32_16x16x32_bf16 v[82:85], v[202:205], v[228:231], v[82:85]
	v_mfma_f32_16x16x32_bf16 v[70:73], v[194:197], v[236:239], v[70:73]
	v_mfma_f32_16x16x32_bf16 v[66:69], v[202:205], v[236:239], v[66:69]
	s_setprio 0
	s_barrier
	s_add_i32 s33, s59, s46
	v_lshl_add_u64 v[240:241], s[0:1], 0, v[132:133]
	s_mov_b32 m0, s33
	ds_read_b128 v[206:209], v176 offset:16384
	ds_read_b128 v[212:215], v176 offset:17408
	ds_read_b128 v[216:219], v176 offset:18432
	ds_read_b128 v[220:223], v176 offset:19456
	ds_read_b128 v[224:227], v176 offset:20480
	ds_read_b128 v[228:231], v176 offset:21504
	ds_read_b128 v[232:235], v176 offset:22528
	ds_read_b128 v[236:239], v176 offset:23552
	global_load_lds_dwordx4 v[240:241], off
	s_add_i32 m0, s33, 0x2000
	v_lshl_add_u64 v[242:243], s[0:1], 0, v[136:137]
	s_add_u32 s0, s0, s14
	s_addc_u32 s1, s1, s15
	s_add_i32 s33, s61, s46
	global_load_lds_dwordx4 v[242:243], off
	v_lshl_add_u64 v[244:245], s[0:1], 0, v[132:133]
	s_mov_b32 m0, s33
	v_lshl_add_u64 v[246:247], s[0:1], 0, v[136:137]
	global_load_lds_dwordx4 v[244:245], off
	s_add_i32 m0, s33, 0x2000
	v_lshl_add_u64 v[248:249], s[42:43], 0, v[130:131]
	global_load_lds_dwordx4 v[246:247], off
	v_lshl_add_u64 v[250:251], s[42:43], 0, v[134:135]
	s_waitcnt vmcnt(6)
	s_waitcnt lgkmcnt(0)
	s_setprio 1
	s_barrier
; #define PG8_STAGE(bufoff, gbase, voff) do { _Pragma("unroll") for (int _i = 0; _i < 2; ++_i) \
;         __builtin_amdgcn_global_load_lds((const unsigned*)((const char*)(gbase) + (voff)[_i]), (PG8_LAS unsigned*)(lds + (bufoff) + ldsw + _i * 8192), 16, 0, 0); } while (0)
; #define PG8_LDA(dst, b, h) do { _Pragma("unroll") for (int m = 0; m < 4; ++m) { const bf16x8 f0_ = *(const PG8_LAS bf16x8*)(lds + PG8_SA(b, h) + aoff + m * 2048), f1_ = *(const PG8_LAS bf16x8*)(lds + PG8_SA(b, h) + aoff + m * 2048 + 1024); dst[m].set(f0_, f1_); } } while (0)
; #define PG8_LDB(dst, b, h) do { _Pragma("unroll") for (int n = 0; n < 2; ++n) { const bf16x8 f0_ = *(const PG8_LAS bf16x8*)(lds + PG8_SB(b, h) + boff + n * 2048), f1_ = *(const PG8_LAS bf16x8*)(lds + PG8_SB(b, h) + boff + n * 2048 + 1024); dst[n].set(f0_, f1_); } } while (0)
; #define PG8_WAIT_V(n) asm volatile("s_waitcnt vmcnt(" #n ")" ::: "memory")
; #define PG8_WAIT_L(n) asm volatile("s_waitcnt lgkmcnt(" #n ")" ::: "memory")
; #define PG8_BAR __builtin_amdgcn_s_barrier()
; #define PG8_SCHED __builtin_amdgcn_sched_barrier(0)
; template <class Epi, class Sched, bool ALIGN_EPI = false, bool SP2 = false>
; __device__ __forceinline__ void gemm_phase(PG8_LAS unsigned char* lds, const Gemm g, const Sched& S, const Epi& E) {
;     ...
;             PG8_WAIT_V(8); PG8_WAIT_L(0); PG8_BAR; PG8_MMA(1, 0, At, B0); PG8_MMA(1, 1, At, B1); PG8_BAR; PG8_SCHED;
;             PG8_LDB(B0, 1, 0); PG8_LDB(B1, 1, 1); PG8_SCHED; PG8_LDA(At, 1, 0); PG8_STAGE(PG8_SA(0, 1), a2 + hstep, voffA);
;             PG8_WAIT_V(8); PG8_WAIT_L(0); PG8_BAR; PG8_MMA(0, 0, At, B0); PG8_MMA(0, 1, At, B1); PG8_BAR; PG8_SCHED;
	s_waitcnt lgkmcnt(0)
	v_mfma_f32_16x16x32_bf16 v[62:65], v[168:171], v[206:209], v[62:65]
	v_mfma_f32_16x16x32_bf16 v[58:61], v[182:185], v[206:209], v[58:61]
	v_mfma_f32_16x16x32_bf16 v[46:49], v[168:171], v[216:219], v[46:49]
	v_mfma_f32_16x16x32_bf16 v[42:45], v[182:185], v[216:219], v[42:45]
	v_mfma_f32_16x16x32_bf16 v[30:33], v[168:171], v[224:227], v[30:33]
	v_mfma_f32_16x16x32_bf16 v[26:29], v[182:185], v[224:227], v[26:29]
	v_mfma_f32_16x16x32_bf16 v[14:17], v[168:171], v[232:235], v[14:17]
	v_mfma_f32_16x16x32_bf16 v[10:13], v[182:185], v[232:235], v[10:13]
	v_mfma_f32_16x16x32_bf16 v[62:65], v[178:181], v[212:215], v[62:65]
	v_mfma_f32_16x16x32_bf16 v[58:61], v[186:189], v[212:215], v[58:61]
	v_mfma_f32_16x16x32_bf16 v[46:49], v[178:181], v[220:223], v[46:49]
	v_mfma_f32_16x16x32_bf16 v[42:45], v[186:189], v[220:223], v[42:45]
	v_mfma_f32_16x16x32_bf16 v[30:33], v[178:181], v[228:231], v[30:33]
	v_mfma_f32_16x16x32_bf16 v[26:29], v[186:189], v[228:231], v[26:29]
	v_mfma_f32_16x16x32_bf16 v[14:17], v[178:181], v[236:239], v[14:17]
	v_mfma_f32_16x16x32_bf16 v[10:13], v[186:189], v[236:239], v[10:13]
	v_mfma_f32_16x16x32_bf16 v[54:57], v[190:193], v[206:209], v[54:57]
	v_mfma_f32_16x16x32_bf16 v[50:53], v[198:201], v[206:209], v[50:53]
	v_mfma_f32_16x16x32_bf16 v[38:41], v[190:193], v[216:219], v[38:41]
	v_mfma_f32_16x16x32_bf16 v[34:37], v[198:201], v[216:219], v[34:37]
	v_mfma_f32_16x16x32_bf16 v[22:25], v[190:193], v[224:227], v[22:25]
	v_mfma_f32_16x16x32_bf16 v[18:21], v[198:201], v[224:227], v[18:21]
	v_mfma_f32_16x16x32_bf16 v[6:9], v[190:193], v[232:235], v[6:9]
	v_mfma_f32_16x16x32_bf16 v[2:5], v[198:201], v[232:235], v[2:5]
	v_mfma_f32_16x16x32_bf16 v[54:57], v[194:197], v[212:215], v[54:57]
	v_mfma_f32_16x16x32_bf16 v[50:53], v[202:205], v[212:215], v[50:53]
	v_mfma_f32_16x16x32_bf16 v[38:41], v[194:197], v[220:223], v[38:41]
	v_mfma_f32_16x16x32_bf16 v[34:37], v[202:205], v[220:223], v[34:37]
	v_mfma_f32_16x16x32_bf16 v[22:25], v[194:197], v[228:231], v[22:25]
	v_mfma_f32_16x16x32_bf16 v[18:21], v[202:205], v[228:231], v[18:21]
	v_mfma_f32_16x16x32_bf16 v[6:9], v[194:197], v[236:239], v[6:9]
	v_mfma_f32_16x16x32_bf16 v[2:5], v[202:205], v[236:239], v[2:5]
	s_setprio 0
	s_barrier
	s_add_i32 s33, 0, 0x18000
	s_add_i32 s76, 0, 0x1c000
	v_add_u32_e32 v186, s33, v173
	v_add_u32_e32 v202, s76, v173
	ds_read_b128 v[168:171], v186
	ds_read_b128 v[178:181], v186 offset:1024
	ds_read_b128 v[182:185], v186 offset:2048
	ds_read_b128 v[186:189], v186 offset:3072
	ds_read_b128 v[190:193], v202
	ds_read_b128 v[194:197], v202 offset:1024
	ds_read_b128 v[198:201], v202 offset:2048
	ds_read_b128 v[202:205], v202 offset:3072
	s_add_u32 s0, s42, s12
	s_addc_u32 s1, s43, s13
	s_mov_b32 m0, s49
	v_lshl_add_u64 v[252:253], s[0:1], 0, v[130:131]
	ds_read_b128 v[206:209], v176 offset:32768
	ds_read_b128 v[212:215], v176 offset:33792
	ds_read_b128 v[216:219], v176 offset:34816
	ds_read_b128 v[220:223], v176 offset:35840
	ds_read_b128 v[224:227], v176 offset:36864
	ds_read_b128 v[228:231], v176 offset:37888
	ds_read_b128 v[232:235], v176 offset:38912
	ds_read_b128 v[236:239], v176 offset:39936
	s_mov_b32 m0, s47
	s_nop 0
	global_load_lds_dwordx4 v[248:249], off
	s_mov_b32 m0, s48
	s_nop 0
	global_load_lds_dwordx4 v[250:251], off
	s_mov_b32 m0, s49
	s_nop 0
	global_load_lds_dwordx4 v[252:253], off
	v_lshl_add_u64 v[252:253], s[0:1], 0, v[134:135]
	s_mov_b32 m0, s50
	s_nop 0
	global_load_lds_dwordx4 v[252:253], off
	s_waitcnt vmcnt(8)
	s_waitcnt lgkmcnt(0)
	s_setprio 1
	s_barrier
; #define PG8_STAGE(bufoff, gbase, voff) do { _Pragma("unroll") for (int _i = 0; _i < 2; ++_i) \
;         __builtin_amdgcn_global_load_lds((const unsigned*)((const char*)(gbase) + (voff)[_i]), (PG8_LAS unsigned*)(lds + (bufoff) + ldsw + _i * 8192), 16, 0, 0); } while (0)
; #define PG8_LDA(dst, b, h) do { _Pragma("unroll") for (int m = 0; m < 4; ++m) { const bf16x8 f0_ = *(const PG8_LAS bf16x8*)(lds + PG8_SA(b, h) + aoff + m * 2048), f1_ = *(const PG8_LAS bf16x8*)(lds + PG8_SA(b, h) + aoff + m * 2048 + 1024); dst[m].set(f0_, f1_); } } while (0)
; #define PG8_LDB(dst, b, h) do { _Pragma("unroll") for (int n = 0; n < 2; ++n) { const bf16x8 f0_ = *(const PG8_LAS bf16x8*)(lds + PG8_SB(b, h) + boff + n * 2048), f1_ = *(const PG8_LAS bf16x8*)(lds + PG8_SB(b, h) + boff + n * 2048 + 1024); dst[n].set(f0_, f1_); } } while (0)
; #define PG8_WAIT_V(n) asm volatile("s_waitcnt vmcnt(" #n ")" ::: "memory")
; #define PG8_WAIT_L(n) asm volatile("s_waitcnt lgkmcnt(" #n ")" ::: "memory")
; #define PG8_BAR __builtin_amdgcn_s_barrier()
; #define PG8_SCHED __builtin_amdgcn_sched_barrier(0)
; template <class Epi, class Sched, bool ALIGN_EPI = false, bool SP2 = false>
; __device__ __forceinline__ void gemm_phase(PG8_LAS unsigned char* lds, const Gemm g, const Sched& S, const Epi& E) {
;     ...
;         for (int t = 0; t < nt; t += 2) {
;             if constexpr (Epi::MIDK) { if (t == (nt >> 1)) E.mid(acc, cur, wr, wc, fr, fq); }
;             const bool last = (t == nt - 2);
;             const char* a1 = cA + (size_t)(t + 1) * kstep;
;             const char* a2 = last ? nA : cA + (size_t)(t + 2) * kstep; const char* b2 = last ? nB : cB + (size_t)(t + 2) * kstep;
;             const char* a3 = a2 + kstep; const char* b3 = b2 + kstep;
;     ...
;             PG8_LDB(B0, 1, 0); PG8_LDB(B1, 1, 1); PG8_SCHED; PG8_LDA(At, 1, 0); PG8_STAGE(PG8_SA(0, 1), a2 + hstep, voffA);
;             PG8_WAIT_V(8); PG8_WAIT_L(0); PG8_BAR; PG8_MMA(0, 0, At, B0); PG8_MMA(0, 1, At, B1); PG8_BAR; PG8_SCHED;
;             PG8_LDA(At, 1, 1); PG8_STAGE(PG8_SB(1, 0), b3, voffB); PG8_STAGE(PG8_SB(1, 1), b3 + hstepB, voffB); PG8_STAGE(PG8_SA(1, 0), a3, voffA);
;             PG8_WAIT_V(8); PG8_WAIT_L(0); PG8_BAR; PG8_MMA(1, 0, At, B0); PG8_MMA(1, 1, At, B1); PG8_BAR; PG8_SCHED;
	s_waitcnt lgkmcnt(0)
	v_mfma_f32_16x16x32_bf16 v[126:129], v[168:171], v[206:209], v[126:129]
	v_mfma_f32_16x16x32_bf16 v[122:125], v[182:185], v[206:209], v[122:125]
	v_mfma_f32_16x16x32_bf16 v[110:113], v[168:171], v[216:219], v[110:113]
	v_mfma_f32_16x16x32_bf16 v[106:109], v[182:185], v[216:219], v[106:109]
	v_mfma_f32_16x16x32_bf16 v[94:97], v[168:171], v[224:227], v[94:97]
	v_mfma_f32_16x16x32_bf16 v[90:93], v[182:185], v[224:227], v[90:93]
	v_mfma_f32_16x16x32_bf16 v[78:81], v[168:171], v[232:235], v[78:81]
	v_mfma_f32_16x16x32_bf16 v[74:77], v[182:185], v[232:235], v[74:77]
	v_mfma_f32_16x16x32_bf16 v[126:129], v[178:181], v[212:215], v[126:129]
	v_mfma_f32_16x16x32_bf16 v[122:125], v[186:189], v[212:215], v[122:125]
	v_mfma_f32_16x16x32_bf16 v[110:113], v[178:181], v[220:223], v[110:113]
	v_mfma_f32_16x16x32_bf16 v[106:109], v[186:189], v[220:223], v[106:109]
	v_mfma_f32_16x16x32_bf16 v[94:97], v[178:181], v[228:231], v[94:97]
	v_mfma_f32_16x16x32_bf16 v[90:93], v[186:189], v[228:231], v[90:93]
	v_mfma_f32_16x16x32_bf16 v[78:81], v[178:181], v[236:239], v[78:81]
	v_mfma_f32_16x16x32_bf16 v[74:77], v[186:189], v[236:239], v[74:77]
	v_mfma_f32_16x16x32_bf16 v[118:121], v[190:193], v[206:209], v[118:121]
	v_mfma_f32_16x16x32_bf16 v[114:117], v[198:201], v[206:209], v[114:117]
	v_mfma_f32_16x16x32_bf16 v[102:105], v[190:193], v[216:219], v[102:105]
	v_mfma_f32_16x16x32_bf16 v[98:101], v[198:201], v[216:219], v[98:101]
	v_mfma_f32_16x16x32_bf16 v[86:89], v[190:193], v[224:227], v[86:89]
	v_mfma_f32_16x16x32_bf16 v[82:85], v[198:201], v[224:227], v[82:85]
	v_mfma_f32_16x16x32_bf16 v[70:73], v[190:193], v[232:235], v[70:73]
	v_mfma_f32_16x16x32_bf16 v[66:69], v[198:201], v[232:235], v[66:69]
	v_mfma_f32_16x16x32_bf16 v[118:121], v[194:197], v[212:215], v[118:121]
	v_mfma_f32_16x16x32_bf16 v[114:117], v[202:205], v[212:215], v[114:117]
	v_mfma_f32_16x16x32_bf16 v[102:105], v[194:197], v[220:223], v[102:105]
	v_mfma_f32_16x16x32_bf16 v[98:101], v[202:205], v[220:223], v[98:101]
	v_mfma_f32_16x16x32_bf16 v[86:89], v[194:197], v[228:231], v[86:89]
	v_mfma_f32_16x16x32_bf16 v[82:85], v[202:205], v[228:231], v[82:85]
	v_mfma_f32_16x16x32_bf16 v[70:73], v[194:197], v[236:239], v[70:73]
	v_mfma_f32_16x16x32_bf16 v[66:69], v[202:205], v[236:239], v[66:69]
	s_setprio 0
	s_barrier
	s_add_i32 s0, s33, s46
	v_lshl_add_u64 v[240:241], v[240:241], 0, s[26:27]
	s_mov_b32 m0, s0
	ds_read_b128 v[206:209], v176 offset:49152
	ds_read_b128 v[212:215], v176 offset:50176
	ds_read_b128 v[216:219], v176 offset:51200
	ds_read_b128 v[220:223], v176 offset:52224
	ds_read_b128 v[224:227], v176 offset:53248
	ds_read_b128 v[228:231], v176 offset:54272
	ds_read_b128 v[232:235], v176 offset:55296
	ds_read_b128 v[236:239], v176 offset:56320
	global_load_lds_dwordx4 v[240:241], off
	v_lshl_add_u64 v[240:241], v[242:243], 0, s[26:27]
	s_add_i32 m0, s0, 0x2000
	s_add_i32 s0, s76, s46
	global_load_lds_dwordx4 v[240:241], off
	v_lshl_add_u64 v[240:241], v[244:245], 0, s[26:27]
	s_mov_b32 m0, s0
	s_nop 0
	global_load_lds_dwordx4 v[240:241], off
	v_lshl_add_u64 v[240:241], v[246:247], 0, s[26:27]
	s_add_i32 m0, s0, 0x2000
	s_nop 0
	global_load_lds_dwordx4 v[240:241], off
	v_lshl_add_u64 v[240:241], v[248:249], 0, s[26:27]
	s_mov_b32 m0, s52
	s_nop 0
	global_load_lds_dwordx4 v[240:241], off
	v_lshl_add_u64 v[240:241], v[250:251], 0, s[26:27]
	s_mov_b32 m0, s53
	s_nop 0
	global_load_lds_dwordx4 v[240:241], off
	s_waitcnt vmcnt(6)
	s_waitcnt lgkmcnt(0)
	s_setprio 1
	s_barrier
	s_waitcnt lgkmcnt(0)
	v_mfma_f32_16x16x32_bf16 v[62:65], v[168:171], v[206:209], v[62:65]
	v_mfma_f32_16x16x32_bf16 v[58:61], v[182:185], v[206:209], v[58:61]
	v_mfma_f32_16x16x32_bf16 v[46:49], v[168:171], v[216:219], v[46:49]
	v_mfma_f32_16x16x32_bf16 v[42:45], v[182:185], v[216:219], v[42:45]
	v_mfma_f32_16x16x32_bf16 v[30:33], v[168:171], v[224:227], v[30:33]
	v_mfma_f32_16x16x32_bf16 v[26:29], v[182:185], v[224:227], v[26:29]
	v_mfma_f32_16x16x32_bf16 v[14:17], v[168:171], v[232:235], v[14:17]
	v_mfma_f32_16x16x32_bf16 v[10:13], v[182:185], v[232:235], v[10:13]
	v_mfma_f32_16x16x32_bf16 v[62:65], v[178:181], v[212:215], v[62:65]
	v_mfma_f32_16x16x32_bf16 v[58:61], v[186:189], v[212:215], v[58:61]
	v_mfma_f32_16x16x32_bf16 v[46:49], v[178:181], v[220:223], v[46:49]
	v_mfma_f32_16x16x32_bf16 v[42:45], v[186:189], v[220:223], v[42:45]
	v_mfma_f32_16x16x32_bf16 v[30:33], v[178:181], v[228:231], v[30:33]
	v_mfma_f32_16x16x32_bf16 v[26:29], v[186:189], v[228:231], v[26:29]
	v_mfma_f32_16x16x32_bf16 v[14:17], v[178:181], v[236:239], v[14:17]
	v_mfma_f32_16x16x32_bf16 v[10:13], v[186:189], v[236:239], v[10:13]
	v_mfma_f32_16x16x32_bf16 v[54:57], v[190:193], v[206:209], v[54:57]
	v_mfma_f32_16x16x32_bf16 v[50:53], v[198:201], v[206:209], v[50:53]
	v_mfma_f32_16x16x32_bf16 v[38:41], v[190:193], v[216:219], v[38:41]
	v_mfma_f32_16x16x32_bf16 v[34:37], v[198:201], v[216:219], v[34:37]
	v_mfma_f32_16x16x32_bf16 v[22:25], v[190:193], v[224:227], v[22:25]
	v_mfma_f32_16x16x32_bf16 v[18:21], v[198:201], v[224:227], v[18:21]
	v_mfma_f32_16x16x32_bf16 v[6:9], v[190:193], v[232:235], v[6:9]
	v_mfma_f32_16x16x32_bf16 v[2:5], v[198:201], v[232:235], v[2:5]
	v_mfma_f32_16x16x32_bf16 v[54:57], v[194:197], v[212:215], v[54:57]
	v_mfma_f32_16x16x32_bf16 v[50:53], v[202:205], v[212:215], v[50:53]
	v_mfma_f32_16x16x32_bf16 v[38:41], v[194:197], v[220:223], v[38:41]
	v_mfma_f32_16x16x32_bf16 v[34:37], v[202:205], v[220:223], v[34:37]
	v_mfma_f32_16x16x32_bf16 v[22:25], v[194:197], v[228:231], v[22:25]
	v_mfma_f32_16x16x32_bf16 v[18:21], v[202:205], v[228:231], v[18:21]
	v_mfma_f32_16x16x32_bf16 v[6:9], v[194:197], v[236:239], v[6:9]
	v_mfma_f32_16x16x32_bf16 v[2:5], v[202:205], v[236:239], v[2:5]
	s_setprio 0
	s_barrier
	s_add_u32 s40, s40, 0x100
	s_addc_u32 s41, s41, 0
	s_cmp_ge_i32 s75, s54
	s_cbranch_scc0 .LBB0_982

; #define PG8_STAGE(bufoff, gbase, voff) do { _Pragma("unroll") for (int _i = 0; _i < 2; ++_i) \
;         __builtin_amdgcn_global_load_lds((const unsigned*)((const char*)(gbase) + (voff)[_i]), (PG8_LAS unsigned*)(lds + (bufoff) + ldsw + _i * 8192), 16, 0, 0); } while (0)
; #define PG8_LDA(dst, b, h) do { _Pragma("unroll") for (int m = 0; m < 4; ++m) { const bf16x8 f0_ = *(const PG8_LAS bf16x8*)(lds + PG8_SA(b, h) + aoff + m * 2048), f1_ = *(const PG8_LAS bf16x8*)(lds + PG8_SA(b, h) + aoff + m * 2048 + 1024); dst[m].set(f0_, f1_); } } while (0)
; #define PG8_LDB(dst, b, h) do { _Pragma("unroll") for (int n = 0; n < 2; ++n) { const bf16x8 f0_ = *(const PG8_LAS bf16x8*)(lds + PG8_SB(b, h) + boff + n * 2048), f1_ = *(const PG8_LAS bf16x8*)(lds + PG8_SB(b, h) + boff + n * 2048 + 1024); dst[n].set(f0_, f1_); } } while (0)
; #define PG8_WAIT_V(n) asm volatile("s_waitcnt vmcnt(" #n ")" ::: "memory")
; #define PG8_WAIT_L(n) asm volatile("s_waitcnt lgkmcnt(" #n ")" ::: "memory")
; #define PG8_BAR __builtin_amdgcn_s_barrier()
; #define PG8_SCHED __builtin_amdgcn_sched_barrier(0)
; template <class Epi, class Sched, bool ALIGN_EPI = false, bool SP2 = false>
; __device__ __forceinline__ void gemm_phase(PG8_LAS unsigned char* lds, const Gemm g, const Sched& S, const Epi& E) {
;     ...
;             PG8_LDB(B0, 0, 0); PG8_LDB(B1, 0, 1); PG8_SCHED; PG8_LDA(At, 0, 0); PG8_STAGE(PG8_SA(1, 1), a1 + hstep, voffA);
;             PG8_WAIT_V(8); PG8_WAIT_L(0); PG8_BAR; PG8_MMA(0, 0, At, B0); PG8_MMA(0, 1, At, B1); PG8_BAR; PG8_SCHED;
;             PG8_LDA(At, 0, 1); PG8_STAGE(PG8_SB(0, 0), b2, voffB); PG8_STAGE(PG8_SB(0, 1), b2 + hstepB, voffB); PG8_STAGE(PG8_SA(0, 0), a2, voffA);
;             PG8_WAIT_V(8); PG8_WAIT_L(0); PG8_BAR; PG8_MMA(1, 0, At, B0); PG8_MMA(1, 1, At, B1); PG8_BAR; PG8_SCHED;
.Lkr2_a:
	v_lshl_add_u64 v[224:225], s[56:57], 0, v[176:177]
	s_add_i32 m0, s67, 0xc000
	ds_read_b128 v[162:165], v195
	ds_read_b128 v[186:189], v195 offset:1024
	ds_read_b128 v[198:201], v195 offset:2048
	ds_read_b128 v[202:205], v195 offset:3072
	ds_read_b128 v[206:209], v195 offset:4096
	ds_read_b128 v[212:215], v195 offset:5120
	ds_read_b128 v[216:219], v195 offset:6144
	ds_read_b128 v[220:223], v195 offset:7168
	global_load_lds_dwordx4 v[224:225], off
	v_lshl_add_u64 v[224:225], s[56:57], 0, v[178:179]
	s_add_i32 m0, s67, 0xe000
	s_nop 0
	global_load_lds_dwordx4 v[224:225], off
	s_waitcnt vmcnt(8)
	s_waitcnt lgkmcnt(0)
	s_setprio 1
	s_barrier
	s_waitcnt lgkmcnt(0)
	v_mfma_f32_16x16x32_bf16 v[126:129], v[130:133], v[162:165], v[126:129]
	v_mfma_f32_16x16x32_bf16 v[122:125], v[138:141], v[162:165], v[122:125]
	v_mfma_f32_16x16x32_bf16 v[58:61], v[130:133], v[198:201], v[58:61]
	v_mfma_f32_16x16x32_bf16 v[62:65], v[138:141], v[198:201], v[62:65]
	v_mfma_f32_16x16x32_bf16 v[106:109], v[130:133], v[206:209], v[106:109]
	v_mfma_f32_16x16x32_bf16 v[110:113], v[138:141], v[206:209], v[110:113]
	v_mfma_f32_16x16x32_bf16 v[98:101], v[130:133], v[216:219], v[98:101]
	v_mfma_f32_16x16x32_bf16 v[102:105], v[138:141], v[216:219], v[102:105]
	v_mfma_f32_16x16x32_bf16 v[126:129], v[134:137], v[186:189], v[126:129]
	v_mfma_f32_16x16x32_bf16 v[122:125], v[142:145], v[186:189], v[122:125]
	v_mfma_f32_16x16x32_bf16 v[58:61], v[134:137], v[202:205], v[58:61]
	v_mfma_f32_16x16x32_bf16 v[62:65], v[142:145], v[202:205], v[62:65]
	v_mfma_f32_16x16x32_bf16 v[106:109], v[134:137], v[212:215], v[106:109]
	v_mfma_f32_16x16x32_bf16 v[110:113], v[142:145], v[212:215], v[110:113]
	v_mfma_f32_16x16x32_bf16 v[98:101], v[134:137], v[220:223], v[98:101]
	v_mfma_f32_16x16x32_bf16 v[102:105], v[142:145], v[220:223], v[102:105]
	v_mfma_f32_16x16x32_bf16 v[118:121], v[146:149], v[162:165], v[118:121]
	v_mfma_f32_16x16x32_bf16 v[114:117], v[154:157], v[162:165], v[114:117]
	v_mfma_f32_16x16x32_bf16 v[50:53], v[146:149], v[198:201], v[50:53]
	v_mfma_f32_16x16x32_bf16 v[54:57], v[154:157], v[198:201], v[54:57]
	v_mfma_f32_16x16x32_bf16 v[90:93], v[146:149], v[206:209], v[90:93]
	v_mfma_f32_16x16x32_bf16 v[94:97], v[154:157], v[206:209], v[94:97]
	v_mfma_f32_16x16x32_bf16 v[74:77], v[146:149], v[216:219], v[74:77]
	v_mfma_f32_16x16x32_bf16 v[78:81], v[154:157], v[216:219], v[78:81]
	v_mfma_f32_16x16x32_bf16 v[118:121], v[150:153], v[186:189], v[118:121]
	v_mfma_f32_16x16x32_bf16 v[114:117], v[158:161], v[186:189], v[114:117]
	v_mfma_f32_16x16x32_bf16 v[50:53], v[150:153], v[202:205], v[50:53]
	v_mfma_f32_16x16x32_bf16 v[54:57], v[158:161], v[202:205], v[54:57]
	v_mfma_f32_16x16x32_bf16 v[90:93], v[150:153], v[212:215], v[90:93]
	v_mfma_f32_16x16x32_bf16 v[94:97], v[158:161], v[212:215], v[94:97]
	v_mfma_f32_16x16x32_bf16 v[74:77], v[150:153], v[220:223], v[74:77]
	v_mfma_f32_16x16x32_bf16 v[78:81], v[158:161], v[220:223], v[78:81]
	s_setprio 0
	s_barrier
	s_add_i32 s33, s82, s66
	v_lshl_add_u64 v[224:225], s[0:1], 0, v[168:169]
	s_mov_b32 m0, s33
	ds_read_b128 v[162:165], v195 offset:16384
	ds_read_b128 v[186:189], v195 offset:17408
	ds_read_b128 v[198:201], v195 offset:18432
	ds_read_b128 v[202:205], v195 offset:19456
	ds_read_b128 v[206:209], v195 offset:20480
	ds_read_b128 v[212:215], v195 offset:21504
	ds_read_b128 v[216:219], v195 offset:22528
	ds_read_b128 v[220:223], v195 offset:23552
	global_load_lds_dwordx4 v[224:225], off
	s_add_i32 m0, s33, 0x2000
	v_lshl_add_u64 v[226:227], s[0:1], 0, v[172:173]
	s_add_u32 s0, s0, s16
	s_addc_u32 s1, s1, s17
	s_add_i32 s33, s83, s66
	global_load_lds_dwordx4 v[226:227], off
	v_lshl_add_u64 v[228:229], s[0:1], 0, v[168:169]
	s_mov_b32 m0, s33
	v_lshl_add_u64 v[230:231], s[0:1], 0, v[172:173]
	global_load_lds_dwordx4 v[228:229], off
	s_add_i32 m0, s33, 0x2000
	v_lshl_add_u64 v[232:233], s[58:59], 0, v[166:167]
	global_load_lds_dwordx4 v[230:231], off
	v_lshl_add_u64 v[234:235], s[58:59], 0, v[170:171]
	s_waitcnt vmcnt(6)
	s_waitcnt lgkmcnt(0)
	s_setprio 1
	s_barrier
	s_waitcnt lgkmcnt(0)
	v_mfma_f32_16x16x32_bf16 v[82:85], v[130:133], v[162:165], v[82:85]
	v_mfma_f32_16x16x32_bf16 v[86:89], v[138:141], v[162:165], v[86:89]
	v_mfma_f32_16x16x32_bf16 v[46:49], v[130:133], v[198:201], v[46:49]
	v_mfma_f32_16x16x32_bf16 v[42:45], v[138:141], v[198:201], v[42:45]
	v_mfma_f32_16x16x32_bf16 v[30:33], v[130:133], v[206:209], v[30:33]
	v_mfma_f32_16x16x32_bf16 v[26:29], v[138:141], v[206:209], v[26:29]
	v_mfma_f32_16x16x32_bf16 v[14:17], v[130:133], v[216:219], v[14:17]
	v_mfma_f32_16x16x32_bf16 v[6:9], v[138:141], v[216:219], v[6:9]
	v_mfma_f32_16x16x32_bf16 v[82:85], v[134:137], v[186:189], v[82:85]
	v_mfma_f32_16x16x32_bf16 v[86:89], v[142:145], v[186:189], v[86:89]
	v_mfma_f32_16x16x32_bf16 v[46:49], v[134:137], v[202:205], v[46:49]
	v_mfma_f32_16x16x32_bf16 v[42:45], v[142:145], v[202:205], v[42:45]
	v_mfma_f32_16x16x32_bf16 v[30:33], v[134:137], v[212:215], v[30:33]
	v_mfma_f32_16x16x32_bf16 v[26:29], v[142:145], v[212:215], v[26:29]
	v_mfma_f32_16x16x32_bf16 v[14:17], v[134:137], v[220:223], v[14:17]
	v_mfma_f32_16x16x32_bf16 v[6:9], v[142:145], v[220:223], v[6:9]
	v_mfma_f32_16x16x32_bf16 v[66:69], v[146:149], v[162:165], v[66:69]
	v_mfma_f32_16x16x32_bf16 v[70:73], v[154:157], v[162:165], v[70:73]
	v_mfma_f32_16x16x32_bf16 v[38:41], v[146:149], v[198:201], v[38:41]
	v_mfma_f32_16x16x32_bf16 v[34:37], v[154:157], v[198:201], v[34:37]
	v_mfma_f32_16x16x32_bf16 v[22:25], v[146:149], v[206:209], v[22:25]
	v_mfma_f32_16x16x32_bf16 v[18:21], v[154:157], v[206:209], v[18:21]
	v_mfma_f32_16x16x32_bf16 v[10:13], v[146:149], v[216:219], v[10:13]
	v_mfma_f32_16x16x32_bf16 v[2:5], v[154:157], v[216:219], v[2:5]
	v_mfma_f32_16x16x32_bf16 v[66:69], v[150:153], v[186:189], v[66:69]
	v_mfma_f32_16x16x32_bf16 v[70:73], v[158:161], v[186:189], v[70:73]
	v_mfma_f32_16x16x32_bf16 v[38:41], v[150:153], v[202:205], v[38:41]
	v_mfma_f32_16x16x32_bf16 v[34:37], v[158:161], v[202:205], v[34:37]
	v_mfma_f32_16x16x32_bf16 v[22:25], v[150:153], v[212:215], v[22:25]
	v_mfma_f32_16x16x32_bf16 v[18:21], v[158:161], v[212:215], v[18:21]
	v_mfma_f32_16x16x32_bf16 v[10:13], v[150:153], v[220:223], v[10:13]
	v_mfma_f32_16x16x32_bf16 v[2:5], v[158:161], v[220:223], v[2:5]
	s_setprio 0
	s_barrier
; #define PG8_STAGE(bufoff, gbase, voff) do { _Pragma("unroll") for (int _i = 0; _i < 2; ++_i) \
;         __builtin_amdgcn_global_load_lds((const unsigned*)((const char*)(gbase) + (voff)[_i]), (PG8_LAS unsigned*)(lds + (bufoff) + ldsw + _i * 8192), 16, 0, 0); } while (0)
; #define PG8_LDA(dst, b, h) do { _Pragma("unroll") for (int m = 0; m < 4; ++m) { const bf16x8 f0_ = *(const PG8_LAS bf16x8*)(lds + PG8_SA(b, h) + aoff + m * 2048), f1_ = *(const PG8_LAS bf16x8*)(lds + PG8_SA(b, h) + aoff + m * 2048 + 1024); dst[m].set(f0_, f1_); } } while (0)
; #define PG8_LDB(dst, b, h) do { _Pragma("unroll") for (int n = 0; n < 2; ++n) { const bf16x8 f0_ = *(const PG8_LAS bf16x8*)(lds + PG8_SB(b, h) + boff + n * 2048), f1_ = *(const PG8_LAS bf16x8*)(lds + PG8_SB(b, h) + boff + n * 2048 + 1024); dst[n].set(f0_, f1_); } } while (0)
; #define PG8_WAIT_V(n) asm volatile("s_waitcnt vmcnt(" #n ")" ::: "memory")
; #define PG8_WAIT_L(n) asm volatile("s_waitcnt lgkmcnt(" #n ")" ::: "memory")
; #define PG8_BAR __builtin_amdgcn_s_barrier()
; #define PG8_SCHED __builtin_amdgcn_sched_barrier(0)
; template <class Epi, class Sched, bool ALIGN_EPI = false, bool SP2 = false>
; __device__ __forceinline__ void gemm_phase(PG8_LAS unsigned char* lds, const Gemm g, const Sched& S, const Epi& E) {
;     ...
;             PG8_WAIT_V(8); PG8_WAIT_L(0); PG8_BAR; PG8_MMA(1, 0, At, B0); PG8_MMA(1, 1, At, B1); PG8_BAR; PG8_SCHED;
;             PG8_LDB(B0, 1, 0); PG8_LDB(B1, 1, 1); PG8_SCHED; PG8_LDA(At, 1, 0); PG8_STAGE(PG8_SA(0, 1), a2 + hstep, voffA);
;             PG8_WAIT_V(8); PG8_WAIT_L(0); PG8_BAR; PG8_MMA(0, 0, At, B0); PG8_MMA(0, 1, At, B1); PG8_BAR; PG8_SCHED;
;             PG8_LDA(At, 1, 1); PG8_STAGE(PG8_SB(1, 0), b3, voffB); PG8_STAGE(PG8_SB(1, 1), b3 + hstepB, voffB); PG8_STAGE(PG8_SA(1, 0), a3, voffA);
	s_add_i32 s33, 0, 0x18000
	s_add_i32 s96, 0, 0x1c000
	v_add_u32_e32 v142, s33, v190
	v_add_u32_e32 v158, s96, v190
	ds_read_b128 v[130:133], v142
	ds_read_b128 v[134:137], v142 offset:1024
	ds_read_b128 v[138:141], v142 offset:2048
	ds_read_b128 v[142:145], v142 offset:3072
	ds_read_b128 v[146:149], v158
	ds_read_b128 v[150:153], v158 offset:1024
	ds_read_b128 v[154:157], v158 offset:2048
	ds_read_b128 v[158:161], v158 offset:3072
	s_add_u32 s0, s58, s14
	s_addc_u32 s1, s59, s15
	s_mov_b32 m0, s71
	v_lshl_add_u64 v[236:237], s[0:1], 0, v[166:167]
	ds_read_b128 v[162:165], v195 offset:32768
	ds_read_b128 v[186:189], v195 offset:33792
	ds_read_b128 v[198:201], v195 offset:34816
	ds_read_b128 v[202:205], v195 offset:35840
	ds_read_b128 v[206:209], v195 offset:36864
	ds_read_b128 v[212:215], v195 offset:37888
	ds_read_b128 v[216:219], v195 offset:38912
	ds_read_b128 v[220:223], v195 offset:39936
	s_mov_b32 m0, s67
	s_nop 0
	global_load_lds_dwordx4 v[232:233], off
	s_mov_b32 m0, s69
	s_nop 0
	global_load_lds_dwordx4 v[234:235], off
	s_mov_b32 m0, s71
	s_nop 0
	global_load_lds_dwordx4 v[236:237], off
	v_lshl_add_u64 v[236:237], s[0:1], 0, v[170:171]
	s_mov_b32 m0, s73
	s_nop 0
	global_load_lds_dwordx4 v[236:237], off
	s_waitcnt vmcnt(8)
	s_waitcnt lgkmcnt(0)
	s_setprio 1
	s_barrier
	s_waitcnt lgkmcnt(0)
	v_mfma_f32_16x16x32_bf16 v[126:129], v[130:133], v[162:165], v[126:129]
	v_mfma_f32_16x16x32_bf16 v[122:125], v[138:141], v[162:165], v[122:125]
	v_mfma_f32_16x16x32_bf16 v[58:61], v[130:133], v[198:201], v[58:61]
	v_mfma_f32_16x16x32_bf16 v[62:65], v[138:141], v[198:201], v[62:65]
	v_mfma_f32_16x16x32_bf16 v[106:109], v[130:133], v[206:209], v[106:109]
	v_mfma_f32_16x16x32_bf16 v[110:113], v[138:141], v[206:209], v[110:113]
	v_mfma_f32_16x16x32_bf16 v[98:101], v[130:133], v[216:219], v[98:101]
	v_mfma_f32_16x16x32_bf16 v[102:105], v[138:141], v[216:219], v[102:105]
	v_mfma_f32_16x16x32_bf16 v[126:129], v[134:137], v[186:189], v[126:129]
	v_mfma_f32_16x16x32_bf16 v[122:125], v[142:145], v[186:189], v[122:125]
	v_mfma_f32_16x16x32_bf16 v[58:61], v[134:137], v[202:205], v[58:61]
	v_mfma_f32_16x16x32_bf16 v[62:65], v[142:145], v[202:205], v[62:65]
	v_mfma_f32_16x16x32_bf16 v[106:109], v[134:137], v[212:215], v[106:109]
	v_mfma_f32_16x16x32_bf16 v[110:113], v[142:145], v[212:215], v[110:113]
	v_mfma_f32_16x16x32_bf16 v[98:101], v[134:137], v[220:223], v[98:101]
	v_mfma_f32_16x16x32_bf16 v[102:105], v[142:145], v[220:223], v[102:105]
	v_mfma_f32_16x16x32_bf16 v[118:121], v[146:149], v[162:165], v[118:121]
	v_mfma_f32_16x16x32_bf16 v[114:117], v[154:157], v[162:165], v[114:117]
	v_mfma_f32_16x16x32_bf16 v[50:53], v[146:149], v[198:201], v[50:53]
	v_mfma_f32_16x16x32_bf16 v[54:57], v[154:157], v[198:201], v[54:57]
	v_mfma_f32_16x16x32_bf16 v[90:93], v[146:149], v[206:209], v[90:93]
	v_mfma_f32_16x16x32_bf16 v[94:97], v[154:157], v[206:209], v[94:97]
	v_mfma_f32_16x16x32_bf16 v[74:77], v[146:149], v[216:219], v[74:77]
	v_mfma_f32_16x16x32_bf16 v[78:81], v[154:157], v[216:219], v[78:81]
	v_mfma_f32_16x16x32_bf16 v[118:121], v[150:153], v[186:189], v[118:121]
	v_mfma_f32_16x16x32_bf16 v[114:117], v[158:161], v[186:189], v[114:117]
	v_mfma_f32_16x16x32_bf16 v[50:53], v[150:153], v[202:205], v[50:53]
	v_mfma_f32_16x16x32_bf16 v[54:57], v[158:161], v[202:205], v[54:57]
	v_mfma_f32_16x16x32_bf16 v[90:93], v[150:153], v[212:215], v[90:93]
	v_mfma_f32_16x16x32_bf16 v[94:97], v[158:161], v[212:215], v[94:97]
	v_mfma_f32_16x16x32_bf16 v[74:77], v[150:153], v[220:223], v[74:77]
	v_mfma_f32_16x16x32_bf16 v[78:81], v[158:161], v[220:223], v[78:81]
	s_setprio 0
	s_barrier
	s_add_i32 s0, s33, s66
	v_lshl_add_u64 v[224:225], v[224:225], 0, s[28:29]
	s_mov_b32 m0, s0
	ds_read_b128 v[162:165], v195 offset:49152
	ds_read_b128 v[186:189], v195 offset:50176
	ds_read_b128 v[198:201], v195 offset:51200
	ds_read_b128 v[202:205], v195 offset:52224
	ds_read_b128 v[206:209], v195 offset:53248
	ds_read_b128 v[212:215], v195 offset:54272
	ds_read_b128 v[216:219], v195 offset:55296
	ds_read_b128 v[220:223], v195 offset:56320
	global_load_lds_dwordx4 v[224:225], off
	v_lshl_add_u64 v[224:225], v[226:227], 0, s[28:29]
	s_add_i32 m0, s0, 0x2000
	s_add_i32 s0, s96, s66
	global_load_lds_dwordx4 v[224:225], off
	v_lshl_add_u64 v[224:225], v[228:229], 0, s[28:29]
	s_mov_b32 m0, s0
	s_nop 0
	global_load_lds_dwordx4 v[224:225], off
	v_lshl_add_u64 v[224:225], v[230:231], 0, s[28:29]
	s_add_i32 m0, s0, 0x2000
	s_nop 0
	global_load_lds_dwordx4 v[224:225], off
	s_cmp_ge_i32 s95, s76
	s_cbranch_scc0 .Lkr2_b
	v_lshl_add_u64 v[224:225], v[232:233], 0, s[28:29]
	s_mov_b32 m0, s74
	s_nop 0
	global_load_lds_dwordx4 v[224:225], off
	v_lshl_add_u64 v[224:225], v[234:235], 0, s[28:29]
	s_mov_b32 m0, s75
	s_nop 0
	global_load_lds_dwordx4 v[224:225], off
; #define PG8_STAGE(bufoff, gbase, voff) do { _Pragma("unroll") for (int _i = 0; _i < 2; ++_i) \
;         __builtin_amdgcn_global_load_lds((const unsigned*)((const char*)(gbase) + (voff)[_i]), (PG8_LAS unsigned*)(lds + (bufoff) + ldsw + _i * 8192), 16, 0, 0); } while (0)
; #define PG8_LDA(dst, b, h) do { _Pragma("unroll") for (int m = 0; m < 4; ++m) { const bf16x8 f0_ = *(const PG8_LAS bf16x8*)(lds + PG8_SA(b, h) + aoff + m * 2048), f1_ = *(const PG8_LAS bf16x8*)(lds + PG8_SA(b, h) + aoff + m * 2048 + 1024); dst[m].set(f0_, f1_); } } while (0)
; #define PG8_WAIT_V(n) asm volatile("s_waitcnt vmcnt(" #n ")" ::: "memory")
; #define PG8_WAIT_L(n) asm volatile("s_waitcnt lgkmcnt(" #n ")" ::: "memory")
; #define PG8_BAR __builtin_amdgcn_s_barrier()
; #define PG8_SCHED __builtin_amdgcn_sched_barrier(0)
; template <class Epi, class Sched, bool ALIGN_EPI = false, bool SP2 = false>
; __device__ __forceinline__ void gemm_phase(PG8_LAS unsigned char* lds, const Gemm g, const Sched& S, const Epi& E) {
;     ...
;         for (int t = 0; t < nt; t += 2) {
;             if constexpr (Epi::MIDK) { if (t == (nt >> 1)) E.mid(acc, cur, wr, wc, fr, fq); }
;             const bool last = (t == nt - 2);
;             const char* a1 = cA + (size_t)(t + 1) * kstep;
;             const char* a2 = last ? nA : cA + (size_t)(t + 2) * kstep; const char* b2 = last ? nB : cB + (size_t)(t + 2) * kstep;
;             const char* a3 = a2 + kstep; const char* b3 = b2 + kstep;
;     ...
;             PG8_LDA(At, 1, 1); PG8_STAGE(PG8_SB(1, 0), b3, voffB); PG8_STAGE(PG8_SB(1, 1), b3 + hstepB, voffB); PG8_STAGE(PG8_SA(1, 0), a3, voffA);
;             PG8_WAIT_V(8); PG8_WAIT_L(0); PG8_BAR; PG8_MMA(1, 0, At, B0); PG8_MMA(1, 1, At, B1); PG8_BAR; PG8_SCHED;
.Lkr2_b:
	s_waitcnt vmcnt(6)
	s_waitcnt lgkmcnt(0)
	s_setprio 1
	s_barrier
	s_waitcnt lgkmcnt(0)
	v_mfma_f32_16x16x32_bf16 v[82:85], v[130:133], v[162:165], v[82:85]
	v_mfma_f32_16x16x32_bf16 v[86:89], v[138:141], v[162:165], v[86:89]
	v_mfma_f32_16x16x32_bf16 v[46:49], v[130:133], v[198:201], v[46:49]
	v_mfma_f32_16x16x32_bf16 v[42:45], v[138:141], v[198:201], v[42:45]
	v_mfma_f32_16x16x32_bf16 v[30:33], v[130:133], v[206:209], v[30:33]
	v_mfma_f32_16x16x32_bf16 v[26:29], v[138:141], v[206:209], v[26:29]
	v_mfma_f32_16x16x32_bf16 v[14:17], v[130:133], v[216:219], v[14:17]
	v_mfma_f32_16x16x32_bf16 v[6:9], v[138:141], v[216:219], v[6:9]
	v_mfma_f32_16x16x32_bf16 v[82:85], v[134:137], v[186:189], v[82:85]
	v_mfma_f32_16x16x32_bf16 v[86:89], v[142:145], v[186:189], v[86:89]
	v_mfma_f32_16x16x32_bf16 v[46:49], v[134:137], v[202:205], v[46:49]
	v_mfma_f32_16x16x32_bf16 v[42:45], v[142:145], v[202:205], v[42:45]
	v_mfma_f32_16x16x32_bf16 v[30:33], v[134:137], v[212:215], v[30:33]
	v_mfma_f32_16x16x32_bf16 v[26:29], v[142:145], v[212:215], v[26:29]
	v_mfma_f32_16x16x32_bf16 v[14:17], v[134:137], v[220:223], v[14:17]
	v_mfma_f32_16x16x32_bf16 v[6:9], v[142:145], v[220:223], v[6:9]
	v_mfma_f32_16x16x32_bf16 v[66:69], v[146:149], v[162:165], v[66:69]
	v_mfma_f32_16x16x32_bf16 v[70:73], v[154:157], v[162:165], v[70:73]
	v_mfma_f32_16x16x32_bf16 v[38:41], v[146:149], v[198:201], v[38:41]
	v_mfma_f32_16x16x32_bf16 v[34:37], v[154:157], v[198:201], v[34:37]
	v_mfma_f32_16x16x32_bf16 v[22:25], v[146:149], v[206:209], v[22:25]
	v_mfma_f32_16x16x32_bf16 v[18:21], v[154:157], v[206:209], v[18:21]
	v_mfma_f32_16x16x32_bf16 v[10:13], v[146:149], v[216:219], v[10:13]
	v_mfma_f32_16x16x32_bf16 v[2:5], v[154:157], v[216:219], v[2:5]
	v_mfma_f32_16x16x32_bf16 v[66:69], v[150:153], v[186:189], v[66:69]
	v_mfma_f32_16x16x32_bf16 v[70:73], v[158:161], v[186:189], v[70:73]
	v_mfma_f32_16x16x32_bf16 v[38:41], v[150:153], v[202:205], v[38:41]
	v_mfma_f32_16x16x32_bf16 v[34:37], v[158:161], v[202:205], v[34:37]
	v_mfma_f32_16x16x32_bf16 v[22:25], v[150:153], v[212:215], v[22:25]
	v_mfma_f32_16x16x32_bf16 v[18:21], v[158:161], v[212:215], v[18:21]
	v_mfma_f32_16x16x32_bf16 v[10:13], v[150:153], v[220:223], v[10:13]
	v_mfma_f32_16x16x32_bf16 v[2:5], v[158:161], v[220:223], v[2:5]
	s_setprio 0
	s_barrier
	s_add_u32 s56, s56, 0x100
	s_addc_u32 s57, s57, 0
	s_add_u32 s93, s93, 0x100
	s_addc_u32 s94, s94, 0
	s_cmp_ge_i32 s95, s76
	s_cselect_b32 s99, 0, 1
	s_mov_b32 s58, s95
	s_cbranch_scc0 .LBB0_1070
	v_readlane_b32 s94, v254, 5
	v_readlane_b32 s95, v254, 6

; #define PG8_STAGE(bufoff, gbase, voff) do { _Pragma("unroll") for (int _i = 0; _i < 2; ++_i) \
;         __builtin_amdgcn_global_load_lds((const unsigned*)((const char*)(gbase) + (voff)[_i]), (PG8_LAS unsigned*)(lds + (bufoff) + ldsw + _i * 8192), 16, 0, 0); } while (0)
; #define PG8_LDA(dst, b, h) do { _Pragma("unroll") for (int m = 0; m < 4; ++m) { const bf16x8 f0_ = *(const PG8_LAS bf16x8*)(lds + PG8_SA(b, h) + aoff + m * 2048), f1_ = *(const PG8_LAS bf16x8*)(lds + PG8_SA(b, h) + aoff + m * 2048 + 1024); dst[m].set(f0_, f1_); } } while (0)
; #define PG8_LDB(dst, b, h) do { _Pragma("unroll") for (int n = 0; n < 2; ++n) { const bf16x8 f0_ = *(const PG8_LAS bf16x8*)(lds + PG8_SB(b, h) + boff + n * 2048), f1_ = *(const PG8_LAS bf16x8*)(lds + PG8_SB(b, h) + boff + n * 2048 + 1024); dst[n].set(f0_, f1_); } } while (0)
; #define PG8_WAIT_V(n) asm volatile("s_waitcnt vmcnt(" #n ")" ::: "memory")
; #define PG8_WAIT_L(n) asm volatile("s_waitcnt lgkmcnt(" #n ")" ::: "memory")
; #define PG8_BAR __builtin_amdgcn_s_barrier()
; #define PG8_SCHED __builtin_amdgcn_sched_barrier(0)
; template <class Epi, class Sched, bool ALIGN_EPI = false, bool SP2 = false>
; __device__ __forceinline__ void gemm_phase(PG8_LAS unsigned char* lds, const Gemm g, const Sched& S, const Epi& E) {
;     ...
;             PG8_LDB(B0, 0, 0); PG8_LDB(B1, 0, 1); PG8_SCHED; PG8_LDA(At, 0, 0); PG8_STAGE(PG8_SA(1, 1), a1 + hstep, voffA);
;             PG8_WAIT_V(8); PG8_WAIT_L(0); PG8_BAR; PG8_MMA(0, 0, At, B0); PG8_MMA(0, 1, At, B1); PG8_BAR; PG8_SCHED;
;             PG8_LDA(At, 0, 1); PG8_STAGE(PG8_SB(0, 0), b2, voffB); PG8_STAGE(PG8_SB(0, 1), b2 + hstepB, voffB); PG8_STAGE(PG8_SA(0, 0), a2, voffA);
;             PG8_WAIT_V(8); PG8_WAIT_L(0); PG8_BAR; PG8_MMA(1, 0, At, B0); PG8_MMA(1, 1, At, B1); PG8_BAR; PG8_SCHED;
.Lkr3_a:
	v_lshl_add_u64 v[148:149], s[30:31], 0, v[140:141]
	s_add_i32 m0, s40, 0xc000
	ds_read_b128 v[188:191], v154
	ds_read_b128 v[192:195], v154 offset:1024
	ds_read_b128 v[196:199], v154 offset:2048
	ds_read_b128 v[200:203], v154 offset:3072
	ds_read_b128 v[204:207], v154 offset:4096
	ds_read_b128 v[212:215], v154 offset:5120
	ds_read_b128 v[216:219], v154 offset:6144
	ds_read_b128 v[220:223], v154 offset:7168
	global_load_lds_dwordx4 v[148:149], off
	v_lshl_add_u64 v[148:149], s[30:31], 0, v[142:143]
	s_add_i32 m0, s40, 0xe000
	s_nop 0
	global_load_lds_dwordx4 v[148:149], off
	s_waitcnt vmcnt(8)
	s_waitcnt lgkmcnt(0)
	s_setprio 1
	s_barrier
	s_waitcnt lgkmcnt(0)
	v_mfma_f32_16x16x32_bf16 v[126:129], v[156:159], v[188:191], v[126:129]
	v_mfma_f32_16x16x32_bf16 v[122:125], v[164:167], v[188:191], v[122:125]
	v_mfma_f32_16x16x32_bf16 v[110:113], v[156:159], v[196:199], v[110:113]
	v_mfma_f32_16x16x32_bf16 v[106:109], v[164:167], v[196:199], v[106:109]
	v_mfma_f32_16x16x32_bf16 v[94:97], v[156:159], v[204:207], v[94:97]
	v_mfma_f32_16x16x32_bf16 v[90:93], v[164:167], v[204:207], v[90:93]
	v_mfma_f32_16x16x32_bf16 v[78:81], v[156:159], v[216:219], v[78:81]
	v_mfma_f32_16x16x32_bf16 v[74:77], v[164:167], v[216:219], v[74:77]
	v_mfma_f32_16x16x32_bf16 v[126:129], v[160:163], v[192:195], v[126:129]
	v_mfma_f32_16x16x32_bf16 v[122:125], v[168:171], v[192:195], v[122:125]
	v_mfma_f32_16x16x32_bf16 v[110:113], v[160:163], v[200:203], v[110:113]
	v_mfma_f32_16x16x32_bf16 v[106:109], v[168:171], v[200:203], v[106:109]
	v_mfma_f32_16x16x32_bf16 v[94:97], v[160:163], v[212:215], v[94:97]
	v_mfma_f32_16x16x32_bf16 v[90:93], v[168:171], v[212:215], v[90:93]
	v_mfma_f32_16x16x32_bf16 v[78:81], v[160:163], v[220:223], v[78:81]
	v_mfma_f32_16x16x32_bf16 v[74:77], v[168:171], v[220:223], v[74:77]
	v_mfma_f32_16x16x32_bf16 v[118:121], v[172:175], v[188:191], v[118:121]
	v_mfma_f32_16x16x32_bf16 v[114:117], v[180:183], v[188:191], v[114:117]
	v_mfma_f32_16x16x32_bf16 v[102:105], v[172:175], v[196:199], v[102:105]
	v_mfma_f32_16x16x32_bf16 v[98:101], v[180:183], v[196:199], v[98:101]
	v_mfma_f32_16x16x32_bf16 v[86:89], v[172:175], v[204:207], v[86:89]
	v_mfma_f32_16x16x32_bf16 v[82:85], v[180:183], v[204:207], v[82:85]
	v_mfma_f32_16x16x32_bf16 v[70:73], v[172:175], v[216:219], v[70:73]
	v_mfma_f32_16x16x32_bf16 v[66:69], v[180:183], v[216:219], v[66:69]
	v_mfma_f32_16x16x32_bf16 v[118:121], v[176:179], v[192:195], v[118:121]
	v_mfma_f32_16x16x32_bf16 v[114:117], v[184:187], v[192:195], v[114:117]
	v_mfma_f32_16x16x32_bf16 v[102:105], v[176:179], v[200:203], v[102:105]
	v_mfma_f32_16x16x32_bf16 v[98:101], v[184:187], v[200:203], v[98:101]
	v_mfma_f32_16x16x32_bf16 v[86:89], v[176:179], v[212:215], v[86:89]
	v_mfma_f32_16x16x32_bf16 v[82:85], v[184:187], v[212:215], v[82:85]
	v_mfma_f32_16x16x32_bf16 v[70:73], v[176:179], v[220:223], v[70:73]
	v_mfma_f32_16x16x32_bf16 v[66:69], v[184:187], v[220:223], v[66:69]
	s_setprio 0
	s_barrier
	s_add_i32 s33, s52, s39
	v_lshl_add_u64 v[148:149], s[0:1], 0, v[132:133]
	s_mov_b32 m0, s33
	ds_read_b128 v[188:191], v154 offset:16384
	ds_read_b128 v[192:195], v154 offset:17408
	ds_read_b128 v[196:199], v154 offset:18432
	ds_read_b128 v[200:203], v154 offset:19456
	ds_read_b128 v[204:207], v154 offset:20480
	ds_read_b128 v[212:215], v154 offset:21504
	ds_read_b128 v[216:219], v154 offset:22528
	ds_read_b128 v[220:223], v154 offset:23552
	global_load_lds_dwordx4 v[148:149], off
	s_add_i32 m0, s33, 0x2000
	v_lshl_add_u64 v[208:209], s[0:1], 0, v[136:137]
	s_add_u32 s0, s0, s14
	s_addc_u32 s1, s1, s15
	s_add_i32 s33, s53, s39
	global_load_lds_dwordx4 v[208:209], off
	v_lshl_add_u64 v[224:225], s[0:1], 0, v[132:133]
	s_mov_b32 m0, s33
	v_lshl_add_u64 v[226:227], s[0:1], 0, v[136:137]
	global_load_lds_dwordx4 v[224:225], off
	s_add_i32 m0, s33, 0x2000
	v_lshl_add_u64 v[228:229], s[34:35], 0, v[130:131]
	global_load_lds_dwordx4 v[226:227], off
	v_lshl_add_u64 v[230:231], s[34:35], 0, v[134:135]
	s_waitcnt vmcnt(6)
	s_waitcnt lgkmcnt(0)
	s_setprio 1
	s_barrier
	s_waitcnt lgkmcnt(0)
	v_mfma_f32_16x16x32_bf16 v[62:65], v[156:159], v[188:191], v[62:65]
	v_mfma_f32_16x16x32_bf16 v[58:61], v[164:167], v[188:191], v[58:61]
	v_mfma_f32_16x16x32_bf16 v[46:49], v[156:159], v[196:199], v[46:49]
	v_mfma_f32_16x16x32_bf16 v[42:45], v[164:167], v[196:199], v[42:45]
	v_mfma_f32_16x16x32_bf16 v[30:33], v[156:159], v[204:207], v[30:33]
	v_mfma_f32_16x16x32_bf16 v[26:29], v[164:167], v[204:207], v[26:29]
	v_mfma_f32_16x16x32_bf16 v[14:17], v[156:159], v[216:219], v[14:17]
	v_mfma_f32_16x16x32_bf16 v[6:9], v[164:167], v[216:219], v[6:9]
	v_mfma_f32_16x16x32_bf16 v[62:65], v[160:163], v[192:195], v[62:65]
	v_mfma_f32_16x16x32_bf16 v[58:61], v[168:171], v[192:195], v[58:61]
	v_mfma_f32_16x16x32_bf16 v[46:49], v[160:163], v[200:203], v[46:49]
	v_mfma_f32_16x16x32_bf16 v[42:45], v[168:171], v[200:203], v[42:45]
	v_mfma_f32_16x16x32_bf16 v[30:33], v[160:163], v[212:215], v[30:33]
	v_mfma_f32_16x16x32_bf16 v[26:29], v[168:171], v[212:215], v[26:29]
	v_mfma_f32_16x16x32_bf16 v[14:17], v[160:163], v[220:223], v[14:17]
	v_mfma_f32_16x16x32_bf16 v[6:9], v[168:171], v[220:223], v[6:9]
	v_mfma_f32_16x16x32_bf16 v[54:57], v[172:175], v[188:191], v[54:57]
	v_mfma_f32_16x16x32_bf16 v[50:53], v[180:183], v[188:191], v[50:53]
	v_mfma_f32_16x16x32_bf16 v[38:41], v[172:175], v[196:199], v[38:41]
	v_mfma_f32_16x16x32_bf16 v[34:37], v[180:183], v[196:199], v[34:37]
	v_mfma_f32_16x16x32_bf16 v[22:25], v[172:175], v[204:207], v[22:25]
	v_mfma_f32_16x16x32_bf16 v[18:21], v[180:183], v[204:207], v[18:21]
	v_mfma_f32_16x16x32_bf16 v[10:13], v[172:175], v[216:219], v[10:13]
	v_mfma_f32_16x16x32_bf16 v[2:5], v[180:183], v[216:219], v[2:5]
	v_mfma_f32_16x16x32_bf16 v[54:57], v[176:179], v[192:195], v[54:57]
	v_mfma_f32_16x16x32_bf16 v[50:53], v[184:187], v[192:195], v[50:53]
	v_mfma_f32_16x16x32_bf16 v[38:41], v[176:179], v[200:203], v[38:41]
	v_mfma_f32_16x16x32_bf16 v[34:37], v[184:187], v[200:203], v[34:37]
	v_mfma_f32_16x16x32_bf16 v[22:25], v[176:179], v[212:215], v[22:25]
	v_mfma_f32_16x16x32_bf16 v[18:21], v[184:187], v[212:215], v[18:21]
	v_mfma_f32_16x16x32_bf16 v[10:13], v[176:179], v[220:223], v[10:13]
	v_mfma_f32_16x16x32_bf16 v[2:5], v[184:187], v[220:223], v[2:5]
	s_setprio 0
	s_barrier
; #define PG8_STAGE(bufoff, gbase, voff) do { _Pragma("unroll") for (int _i = 0; _i < 2; ++_i) \
;         __builtin_amdgcn_global_load_lds((const unsigned*)((const char*)(gbase) + (voff)[_i]), (PG8_LAS unsigned*)(lds + (bufoff) + ldsw + _i * 8192), 16, 0, 0); } while (0)
; #define PG8_LDA(dst, b, h) do { _Pragma("unroll") for (int m = 0; m < 4; ++m) { const bf16x8 f0_ = *(const PG8_LAS bf16x8*)(lds + PG8_SA(b, h) + aoff + m * 2048), f1_ = *(const PG8_LAS bf16x8*)(lds + PG8_SA(b, h) + aoff + m * 2048 + 1024); dst[m].set(f0_, f1_); } } while (0)
; #define PG8_LDB(dst, b, h) do { _Pragma("unroll") for (int n = 0; n < 2; ++n) { const bf16x8 f0_ = *(const PG8_LAS bf16x8*)(lds + PG8_SB(b, h) + boff + n * 2048), f1_ = *(const PG8_LAS bf16x8*)(lds + PG8_SB(b, h) + boff + n * 2048 + 1024); dst[n].set(f0_, f1_); } } while (0)
; #define PG8_WAIT_V(n) asm volatile("s_waitcnt vmcnt(" #n ")" ::: "memory")
; #define PG8_WAIT_L(n) asm volatile("s_waitcnt lgkmcnt(" #n ")" ::: "memory")
; #define PG8_BAR __builtin_amdgcn_s_barrier()
; #define PG8_SCHED __builtin_amdgcn_sched_barrier(0)
; template <class Epi, class Sched, bool ALIGN_EPI = false, bool SP2 = false>
; __device__ __forceinline__ void gemm_phase(PG8_LAS unsigned char* lds, const Gemm g, const Sched& S, const Epi& E) {
;     ...
;             PG8_LDB(B0, 1, 0); PG8_LDB(B1, 1, 1); PG8_SCHED; PG8_LDA(At, 1, 0); PG8_STAGE(PG8_SA(0, 1), a2 + hstep, voffA);
;             PG8_WAIT_V(8); PG8_WAIT_L(0); PG8_BAR; PG8_MMA(0, 0, At, B0); PG8_MMA(0, 1, At, B1); PG8_BAR; PG8_SCHED;
;             PG8_LDA(At, 1, 1); PG8_STAGE(PG8_SB(1, 0), b3, voffB); PG8_STAGE(PG8_SB(1, 1), b3 + hstepB, voffB); PG8_STAGE(PG8_SA(1, 0), a3, voffA);
	s_add_i32 s33, 0, 0x18000
	s_add_i32 s63, 0, 0x1c000
	v_add_u32_e32 v168, s33, v1
	v_add_u32_e32 v184, s63, v1
	ds_read_b128 v[156:159], v168
	ds_read_b128 v[160:163], v168 offset:1024
	ds_read_b128 v[164:167], v168 offset:2048
	ds_read_b128 v[168:171], v168 offset:3072
	ds_read_b128 v[172:175], v184
	ds_read_b128 v[176:179], v184 offset:1024
	ds_read_b128 v[180:183], v184 offset:2048
	ds_read_b128 v[184:187], v184 offset:3072
	s_add_u32 s0, s34, s12
	s_addc_u32 s1, s35, s13
	s_mov_b32 m0, s42
	v_lshl_add_u64 v[232:233], s[0:1], 0, v[130:131]
	ds_read_b128 v[188:191], v154 offset:32768
	ds_read_b128 v[192:195], v154 offset:33792
	ds_read_b128 v[196:199], v154 offset:34816
	ds_read_b128 v[200:203], v154 offset:35840
	ds_read_b128 v[204:207], v154 offset:36864
	ds_read_b128 v[212:215], v154 offset:37888
	ds_read_b128 v[216:219], v154 offset:38912
	ds_read_b128 v[220:223], v154 offset:39936
	s_mov_b32 m0, s40
	s_nop 0
	global_load_lds_dwordx4 v[228:229], off
	s_mov_b32 m0, s41
	s_nop 0
	global_load_lds_dwordx4 v[230:231], off
	s_mov_b32 m0, s42
	s_nop 0
	global_load_lds_dwordx4 v[232:233], off
	v_lshl_add_u64 v[232:233], s[0:1], 0, v[134:135]
	s_mov_b32 m0, s43
	s_nop 0
	global_load_lds_dwordx4 v[232:233], off
	s_waitcnt vmcnt(8)
	s_waitcnt lgkmcnt(0)
	s_setprio 1
	s_barrier
	s_waitcnt lgkmcnt(0)
	v_mfma_f32_16x16x32_bf16 v[126:129], v[156:159], v[188:191], v[126:129]
	v_mfma_f32_16x16x32_bf16 v[122:125], v[164:167], v[188:191], v[122:125]
	v_mfma_f32_16x16x32_bf16 v[110:113], v[156:159], v[196:199], v[110:113]
	v_mfma_f32_16x16x32_bf16 v[106:109], v[164:167], v[196:199], v[106:109]
	v_mfma_f32_16x16x32_bf16 v[94:97], v[156:159], v[204:207], v[94:97]
	v_mfma_f32_16x16x32_bf16 v[90:93], v[164:167], v[204:207], v[90:93]
	v_mfma_f32_16x16x32_bf16 v[78:81], v[156:159], v[216:219], v[78:81]
	v_mfma_f32_16x16x32_bf16 v[74:77], v[164:167], v[216:219], v[74:77]
	v_mfma_f32_16x16x32_bf16 v[126:129], v[160:163], v[192:195], v[126:129]
	v_mfma_f32_16x16x32_bf16 v[122:125], v[168:171], v[192:195], v[122:125]
	v_mfma_f32_16x16x32_bf16 v[110:113], v[160:163], v[200:203], v[110:113]
	v_mfma_f32_16x16x32_bf16 v[106:109], v[168:171], v[200:203], v[106:109]
	v_mfma_f32_16x16x32_bf16 v[94:97], v[160:163], v[212:215], v[94:97]
	v_mfma_f32_16x16x32_bf16 v[90:93], v[168:171], v[212:215], v[90:93]
	v_mfma_f32_16x16x32_bf16 v[78:81], v[160:163], v[220:223], v[78:81]
	v_mfma_f32_16x16x32_bf16 v[74:77], v[168:171], v[220:223], v[74:77]
	v_mfma_f32_16x16x32_bf16 v[118:121], v[172:175], v[188:191], v[118:121]
	v_mfma_f32_16x16x32_bf16 v[114:117], v[180:183], v[188:191], v[114:117]
	v_mfma_f32_16x16x32_bf16 v[102:105], v[172:175], v[196:199], v[102:105]
	v_mfma_f32_16x16x32_bf16 v[98:101], v[180:183], v[196:199], v[98:101]
	v_mfma_f32_16x16x32_bf16 v[86:89], v[172:175], v[204:207], v[86:89]
	v_mfma_f32_16x16x32_bf16 v[82:85], v[180:183], v[204:207], v[82:85]
	v_mfma_f32_16x16x32_bf16 v[70:73], v[172:175], v[216:219], v[70:73]
	v_mfma_f32_16x16x32_bf16 v[66:69], v[180:183], v[216:219], v[66:69]
	v_mfma_f32_16x16x32_bf16 v[118:121], v[176:179], v[192:195], v[118:121]
	v_mfma_f32_16x16x32_bf16 v[114:117], v[184:187], v[192:195], v[114:117]
	v_mfma_f32_16x16x32_bf16 v[102:105], v[176:179], v[200:203], v[102:105]
	v_mfma_f32_16x16x32_bf16 v[98:101], v[184:187], v[200:203], v[98:101]
	v_mfma_f32_16x16x32_bf16 v[86:89], v[176:179], v[212:215], v[86:89]
	v_mfma_f32_16x16x32_bf16 v[82:85], v[184:187], v[212:215], v[82:85]
	v_mfma_f32_16x16x32_bf16 v[70:73], v[176:179], v[220:223], v[70:73]
	v_mfma_f32_16x16x32_bf16 v[66:69], v[184:187], v[220:223], v[66:69]
	s_setprio 0
	s_barrier
	s_add_i32 s0, s33, s39
	v_lshl_add_u64 v[148:149], v[148:149], 0, s[22:23]
	s_mov_b32 m0, s0
	ds_read_b128 v[188:191], v154 offset:49152
	ds_read_b128 v[192:195], v154 offset:50176
	ds_read_b128 v[196:199], v154 offset:51200
	ds_read_b128 v[200:203], v154 offset:52224
	ds_read_b128 v[204:207], v154 offset:53248
	ds_read_b128 v[212:215], v154 offset:54272
	ds_read_b128 v[216:219], v154 offset:55296
	ds_read_b128 v[220:223], v154 offset:56320
	global_load_lds_dwordx4 v[148:149], off
	v_lshl_add_u64 v[148:149], v[208:209], 0, s[22:23]
	s_add_i32 m0, s0, 0x2000
	s_add_i32 s0, s63, s39
	global_load_lds_dwordx4 v[148:149], off
	v_lshl_add_u64 v[148:149], v[224:225], 0, s[22:23]
	s_mov_b32 m0, s0
	s_nop 0
	global_load_lds_dwordx4 v[148:149], off
	v_lshl_add_u64 v[148:149], v[226:227], 0, s[22:23]
	s_add_i32 m0, s0, 0x2000
	s_nop 0
	global_load_lds_dwordx4 v[148:149], off
	s_cmp_ge_i32 s61, s47
	s_cbranch_scc0 .Lkr3_b
	v_lshl_add_u64 v[148:149], v[228:229], 0, s[22:23]
	s_mov_b32 m0, s45
	s_nop 0
	global_load_lds_dwordx4 v[148:149], off
	v_lshl_add_u64 v[148:149], v[230:231], 0, s[22:23]
	s_mov_b32 m0, s46
	s_nop 0
	global_load_lds_dwordx4 v[148:149], off
; #define PG8_WAIT_V(n) asm volatile("s_waitcnt vmcnt(" #n ")" ::: "memory")
; #define PG8_WAIT_L(n) asm volatile("s_waitcnt lgkmcnt(" #n ")" ::: "memory")
; #define PG8_BAR __builtin_amdgcn_s_barrier()
; #define PG8_SCHED __builtin_amdgcn_sched_barrier(0)
; template <class Epi, class Sched, bool ALIGN_EPI = false, bool SP2 = false>
; __device__ __forceinline__ void gemm_phase(PG8_LAS unsigned char* lds, const Gemm g, const Sched& S, const Epi& E) {
;     ...
;         for (int t = 0; t < nt; t += 2) {
;             if constexpr (Epi::MIDK) { if (t == (nt >> 1)) E.mid(acc, cur, wr, wc, fr, fq); }
;             const bool last = (t == nt - 2);
;             const char* a1 = cA + (size_t)(t + 1) * kstep;
;             const char* a2 = last ? nA : cA + (size_t)(t + 2) * kstep; const char* b2 = last ? nB : cB + (size_t)(t + 2) * kstep;
;             const char* a3 = a2 + kstep; const char* b3 = b2 + kstep;
;     ...
;             PG8_WAIT_V(8); PG8_WAIT_L(0); PG8_BAR; PG8_MMA(1, 0, At, B0); PG8_MMA(1, 1, At, B1); PG8_BAR; PG8_SCHED;
.Lkr3_b:
	s_waitcnt vmcnt(6)
	s_waitcnt lgkmcnt(0)
	s_setprio 1
	s_barrier
	s_waitcnt lgkmcnt(0)
	v_mfma_f32_16x16x32_bf16 v[62:65], v[156:159], v[188:191], v[62:65]
	v_mfma_f32_16x16x32_bf16 v[58:61], v[164:167], v[188:191], v[58:61]
	v_mfma_f32_16x16x32_bf16 v[46:49], v[156:159], v[196:199], v[46:49]
	v_mfma_f32_16x16x32_bf16 v[42:45], v[164:167], v[196:199], v[42:45]
	v_mfma_f32_16x16x32_bf16 v[30:33], v[156:159], v[204:207], v[30:33]
	v_mfma_f32_16x16x32_bf16 v[26:29], v[164:167], v[204:207], v[26:29]
	v_mfma_f32_16x16x32_bf16 v[14:17], v[156:159], v[216:219], v[14:17]
	v_mfma_f32_16x16x32_bf16 v[6:9], v[164:167], v[216:219], v[6:9]
	v_mfma_f32_16x16x32_bf16 v[62:65], v[160:163], v[192:195], v[62:65]
	v_mfma_f32_16x16x32_bf16 v[58:61], v[168:171], v[192:195], v[58:61]
	v_mfma_f32_16x16x32_bf16 v[46:49], v[160:163], v[200:203], v[46:49]
	v_mfma_f32_16x16x32_bf16 v[42:45], v[168:171], v[200:203], v[42:45]
	v_mfma_f32_16x16x32_bf16 v[30:33], v[160:163], v[212:215], v[30:33]
	v_mfma_f32_16x16x32_bf16 v[26:29], v[168:171], v[212:215], v[26:29]
	v_mfma_f32_16x16x32_bf16 v[14:17], v[160:163], v[220:223], v[14:17]
	v_mfma_f32_16x16x32_bf16 v[6:9], v[168:171], v[220:223], v[6:9]
	v_mfma_f32_16x16x32_bf16 v[54:57], v[172:175], v[188:191], v[54:57]
	v_mfma_f32_16x16x32_bf16 v[50:53], v[180:183], v[188:191], v[50:53]
	v_mfma_f32_16x16x32_bf16 v[38:41], v[172:175], v[196:199], v[38:41]
	v_mfma_f32_16x16x32_bf16 v[34:37], v[180:183], v[196:199], v[34:37]
	v_mfma_f32_16x16x32_bf16 v[22:25], v[172:175], v[204:207], v[22:25]
	v_mfma_f32_16x16x32_bf16 v[18:21], v[180:183], v[204:207], v[18:21]
	v_mfma_f32_16x16x32_bf16 v[10:13], v[172:175], v[216:219], v[10:13]
	v_mfma_f32_16x16x32_bf16 v[2:5], v[180:183], v[216:219], v[2:5]
	v_mfma_f32_16x16x32_bf16 v[54:57], v[176:179], v[192:195], v[54:57]
	v_mfma_f32_16x16x32_bf16 v[50:53], v[184:187], v[192:195], v[50:53]
	v_mfma_f32_16x16x32_bf16 v[38:41], v[176:179], v[200:203], v[38:41]
	v_mfma_f32_16x16x32_bf16 v[34:37], v[184:187], v[200:203], v[34:37]
	v_mfma_f32_16x16x32_bf16 v[22:25], v[176:179], v[212:215], v[22:25]
	v_mfma_f32_16x16x32_bf16 v[18:21], v[184:187], v[212:215], v[18:21]
	v_mfma_f32_16x16x32_bf16 v[10:13], v[176:179], v[220:223], v[10:13]
	v_mfma_f32_16x16x32_bf16 v[2:5], v[184:187], v[220:223], v[2:5]
	s_setprio 0
	s_barrier
	s_add_u32 s30, s30, 0x100
	s_addc_u32 s31, s31, 0
	s_add_u32 s58, s58, 0x100
	s_addc_u32 s59, s59, 0
	s_cmp_ge_i32 s61, s47
	s_cselect_b32 s99, 0, 1
	s_mov_b32 s34, s61
	s_cbranch_scc0 .LBB0_1171

; #define PG8_STAGE(bufoff, gbase, voff) do { _Pragma("unroll") for (int _i = 0; _i < 2; ++_i) \
;         __builtin_amdgcn_global_load_lds((const unsigned*)((const char*)(gbase) + (voff)[_i]), (PG8_LAS unsigned*)(lds + (bufoff) + ldsw + _i * 8192), 16, 0, 0); } while (0)
; #define PG8_LDA(dst, b, h) do { _Pragma("unroll") for (int m = 0; m < 4; ++m) { const bf16x8 f0_ = *(const PG8_LAS bf16x8*)(lds + PG8_SA(b, h) + aoff + m * 2048), f1_ = *(const PG8_LAS bf16x8*)(lds + PG8_SA(b, h) + aoff + m * 2048 + 1024); dst[m].set(f0_, f1_); } } while (0)
; #define PG8_LDB(dst, b, h) do { _Pragma("unroll") for (int n = 0; n < 2; ++n) { const bf16x8 f0_ = *(const PG8_LAS bf16x8*)(lds + PG8_SB(b, h) + boff + n * 2048), f1_ = *(const PG8_LAS bf16x8*)(lds + PG8_SB(b, h) + boff + n * 2048 + 1024); dst[n].set(f0_, f1_); } } while (0)
; #define PG8_WAIT_V(n) asm volatile("s_waitcnt vmcnt(" #n ")" ::: "memory")
; #define PG8_WAIT_L(n) asm volatile("s_waitcnt lgkmcnt(" #n ")" ::: "memory")
; #define PG8_BAR __builtin_amdgcn_s_barrier()
; #define PG8_SCHED __builtin_amdgcn_sched_barrier(0)
; template <class Epi, class Sched, bool ALIGN_EPI = false, bool SP2 = false>
; __device__ __forceinline__ void gemm_phase(PG8_LAS unsigned char* lds, const Gemm g, const Sched& S, const Epi& E) {
;     ...
;             PG8_LDB(B0, 0, 0); PG8_LDB(B1, 0, 1); PG8_SCHED; PG8_LDA(At, 0, 0); PG8_STAGE(PG8_SA(1, 1), a1 + hstep, voffA);
;             PG8_WAIT_V(8); PG8_WAIT_L(0); PG8_BAR; PG8_MMA(0, 0, At, B0); PG8_MMA(0, 1, At, B1); PG8_BAR; PG8_SCHED;
;             PG8_LDA(At, 0, 1); PG8_STAGE(PG8_SB(0, 0), b2, voffB); PG8_STAGE(PG8_SB(0, 1), b2 + hstepB, voffB); PG8_STAGE(PG8_SA(0, 0), a2, voffA);
;             PG8_WAIT_V(8); PG8_WAIT_L(0); PG8_BAR; PG8_MMA(1, 0, At, B0); PG8_MMA(1, 1, At, B1); PG8_BAR; PG8_SCHED;
.Lkr4_a:
	v_lshl_add_u64 v[148:149], s[30:31], 0, v[140:141]
	s_add_i32 m0, s40, 0xc000
	ds_read_b128 v[188:191], v154
	ds_read_b128 v[192:195], v154 offset:1024
	ds_read_b128 v[196:199], v154 offset:2048
	ds_read_b128 v[200:203], v154 offset:3072
	ds_read_b128 v[204:207], v154 offset:4096
	ds_read_b128 v[212:215], v154 offset:5120
	ds_read_b128 v[216:219], v154 offset:6144
	ds_read_b128 v[220:223], v154 offset:7168
	global_load_lds_dwordx4 v[148:149], off
	v_lshl_add_u64 v[148:149], s[30:31], 0, v[142:143]
	s_add_i32 m0, s40, 0xe000
	s_nop 0
	global_load_lds_dwordx4 v[148:149], off
	s_waitcnt vmcnt(8)
	s_waitcnt lgkmcnt(0)
	s_setprio 1
	s_barrier
	s_waitcnt lgkmcnt(0)
	v_mfma_f32_16x16x32_bf16 v[126:129], v[156:159], v[188:191], v[126:129]
	v_mfma_f32_16x16x32_bf16 v[122:125], v[164:167], v[188:191], v[122:125]
	v_mfma_f32_16x16x32_bf16 v[110:113], v[156:159], v[196:199], v[110:113]
	v_mfma_f32_16x16x32_bf16 v[106:109], v[164:167], v[196:199], v[106:109]
	v_mfma_f32_16x16x32_bf16 v[94:97], v[156:159], v[204:207], v[94:97]
	v_mfma_f32_16x16x32_bf16 v[90:93], v[164:167], v[204:207], v[90:93]
	v_mfma_f32_16x16x32_bf16 v[78:81], v[156:159], v[216:219], v[78:81]
	v_mfma_f32_16x16x32_bf16 v[74:77], v[164:167], v[216:219], v[74:77]
	v_mfma_f32_16x16x32_bf16 v[126:129], v[160:163], v[192:195], v[126:129]
	v_mfma_f32_16x16x32_bf16 v[122:125], v[168:171], v[192:195], v[122:125]
	v_mfma_f32_16x16x32_bf16 v[110:113], v[160:163], v[200:203], v[110:113]
	v_mfma_f32_16x16x32_bf16 v[106:109], v[168:171], v[200:203], v[106:109]
	v_mfma_f32_16x16x32_bf16 v[94:97], v[160:163], v[212:215], v[94:97]
	v_mfma_f32_16x16x32_bf16 v[90:93], v[168:171], v[212:215], v[90:93]
	v_mfma_f32_16x16x32_bf16 v[78:81], v[160:163], v[220:223], v[78:81]
	v_mfma_f32_16x16x32_bf16 v[74:77], v[168:171], v[220:223], v[74:77]
	v_mfma_f32_16x16x32_bf16 v[118:121], v[172:175], v[188:191], v[118:121]
	v_mfma_f32_16x16x32_bf16 v[114:117], v[180:183], v[188:191], v[114:117]
	v_mfma_f32_16x16x32_bf16 v[102:105], v[172:175], v[196:199], v[102:105]
	v_mfma_f32_16x16x32_bf16 v[98:101], v[180:183], v[196:199], v[98:101]
	v_mfma_f32_16x16x32_bf16 v[86:89], v[172:175], v[204:207], v[86:89]
	v_mfma_f32_16x16x32_bf16 v[82:85], v[180:183], v[204:207], v[82:85]
	v_mfma_f32_16x16x32_bf16 v[70:73], v[172:175], v[216:219], v[70:73]
	v_mfma_f32_16x16x32_bf16 v[66:69], v[180:183], v[216:219], v[66:69]
	v_mfma_f32_16x16x32_bf16 v[118:121], v[176:179], v[192:195], v[118:121]
	v_mfma_f32_16x16x32_bf16 v[114:117], v[184:187], v[192:195], v[114:117]
	v_mfma_f32_16x16x32_bf16 v[102:105], v[176:179], v[200:203], v[102:105]
	v_mfma_f32_16x16x32_bf16 v[98:101], v[184:187], v[200:203], v[98:101]
	v_mfma_f32_16x16x32_bf16 v[86:89], v[176:179], v[212:215], v[86:89]
	v_mfma_f32_16x16x32_bf16 v[82:85], v[184:187], v[212:215], v[82:85]
	v_mfma_f32_16x16x32_bf16 v[70:73], v[176:179], v[220:223], v[70:73]
	v_mfma_f32_16x16x32_bf16 v[66:69], v[184:187], v[220:223], v[66:69]
	s_setprio 0
	s_barrier
	s_add_i32 s33, s52, s39
	v_lshl_add_u64 v[148:149], s[0:1], 0, v[132:133]
	s_mov_b32 m0, s33
	ds_read_b128 v[188:191], v154 offset:16384
	ds_read_b128 v[192:195], v154 offset:17408
	ds_read_b128 v[196:199], v154 offset:18432
	ds_read_b128 v[200:203], v154 offset:19456
	ds_read_b128 v[204:207], v154 offset:20480
	ds_read_b128 v[212:215], v154 offset:21504
	ds_read_b128 v[216:219], v154 offset:22528
	ds_read_b128 v[220:223], v154 offset:23552
	global_load_lds_dwordx4 v[148:149], off
	s_add_i32 m0, s33, 0x2000
	v_lshl_add_u64 v[208:209], s[0:1], 0, v[136:137]
	s_add_u32 s0, s0, s14
	s_addc_u32 s1, s1, s15
	s_add_i32 s33, s53, s39
	global_load_lds_dwordx4 v[208:209], off
	v_lshl_add_u64 v[224:225], s[0:1], 0, v[132:133]
	s_mov_b32 m0, s33
	v_lshl_add_u64 v[226:227], s[0:1], 0, v[136:137]
	global_load_lds_dwordx4 v[224:225], off
	s_add_i32 m0, s33, 0x2000
	v_lshl_add_u64 v[228:229], s[34:35], 0, v[130:131]
	global_load_lds_dwordx4 v[226:227], off
	v_lshl_add_u64 v[230:231], s[34:35], 0, v[134:135]
	s_waitcnt vmcnt(6)
	s_waitcnt lgkmcnt(0)
	s_setprio 1
	s_barrier
	s_waitcnt lgkmcnt(0)
	v_mfma_f32_16x16x32_bf16 v[62:65], v[156:159], v[188:191], v[62:65]
	v_mfma_f32_16x16x32_bf16 v[58:61], v[164:167], v[188:191], v[58:61]
	v_mfma_f32_16x16x32_bf16 v[46:49], v[156:159], v[196:199], v[46:49]
	v_mfma_f32_16x16x32_bf16 v[42:45], v[164:167], v[196:199], v[42:45]
	v_mfma_f32_16x16x32_bf16 v[30:33], v[156:159], v[204:207], v[30:33]
	v_mfma_f32_16x16x32_bf16 v[26:29], v[164:167], v[204:207], v[26:29]
	v_mfma_f32_16x16x32_bf16 v[14:17], v[156:159], v[216:219], v[14:17]
	v_mfma_f32_16x16x32_bf16 v[6:9], v[164:167], v[216:219], v[6:9]
	v_mfma_f32_16x16x32_bf16 v[62:65], v[160:163], v[192:195], v[62:65]
	v_mfma_f32_16x16x32_bf16 v[58:61], v[168:171], v[192:195], v[58:61]
	v_mfma_f32_16x16x32_bf16 v[46:49], v[160:163], v[200:203], v[46:49]
	v_mfma_f32_16x16x32_bf16 v[42:45], v[168:171], v[200:203], v[42:45]
	v_mfma_f32_16x16x32_bf16 v[30:33], v[160:163], v[212:215], v[30:33]
	v_mfma_f32_16x16x32_bf16 v[26:29], v[168:171], v[212:215], v[26:29]
	v_mfma_f32_16x16x32_bf16 v[14:17], v[160:163], v[220:223], v[14:17]
	v_mfma_f32_16x16x32_bf16 v[6:9], v[168:171], v[220:223], v[6:9]
	v_mfma_f32_16x16x32_bf16 v[54:57], v[172:175], v[188:191], v[54:57]
	v_mfma_f32_16x16x32_bf16 v[50:53], v[180:183], v[188:191], v[50:53]
	v_mfma_f32_16x16x32_bf16 v[38:41], v[172:175], v[196:199], v[38:41]
	v_mfma_f32_16x16x32_bf16 v[34:37], v[180:183], v[196:199], v[34:37]
	v_mfma_f32_16x16x32_bf16 v[22:25], v[172:175], v[204:207], v[22:25]
	v_mfma_f32_16x16x32_bf16 v[18:21], v[180:183], v[204:207], v[18:21]
	v_mfma_f32_16x16x32_bf16 v[10:13], v[172:175], v[216:219], v[10:13]
	v_mfma_f32_16x16x32_bf16 v[2:5], v[180:183], v[216:219], v[2:5]
	v_mfma_f32_16x16x32_bf16 v[54:57], v[176:179], v[192:195], v[54:57]
	v_mfma_f32_16x16x32_bf16 v[50:53], v[184:187], v[192:195], v[50:53]
	v_mfma_f32_16x16x32_bf16 v[38:41], v[176:179], v[200:203], v[38:41]
	v_mfma_f32_16x16x32_bf16 v[34:37], v[184:187], v[200:203], v[34:37]
	v_mfma_f32_16x16x32_bf16 v[22:25], v[176:179], v[212:215], v[22:25]
	v_mfma_f32_16x16x32_bf16 v[18:21], v[184:187], v[212:215], v[18:21]
	v_mfma_f32_16x16x32_bf16 v[10:13], v[176:179], v[220:223], v[10:13]
	v_mfma_f32_16x16x32_bf16 v[2:5], v[184:187], v[220:223], v[2:5]
	s_setprio 0
	s_barrier
; #define PG8_STAGE(bufoff, gbase, voff) do { _Pragma("unroll") for (int _i = 0; _i < 2; ++_i) \
;         __builtin_amdgcn_global_load_lds((const unsigned*)((const char*)(gbase) + (voff)[_i]), (PG8_LAS unsigned*)(lds + (bufoff) + ldsw + _i * 8192), 16, 0, 0); } while (0)
; #define PG8_LDA(dst, b, h) do { _Pragma("unroll") for (int m = 0; m < 4; ++m) { const bf16x8 f0_ = *(const PG8_LAS bf16x8*)(lds + PG8_SA(b, h) + aoff + m * 2048), f1_ = *(const PG8_LAS bf16x8*)(lds + PG8_SA(b, h) + aoff + m * 2048 + 1024); dst[m].set(f0_, f1_); } } while (0)
; #define PG8_LDB(dst, b, h) do { _Pragma("unroll") for (int n = 0; n < 2; ++n) { const bf16x8 f0_ = *(const PG8_LAS bf16x8*)(lds + PG8_SB(b, h) + boff + n * 2048), f1_ = *(const PG8_LAS bf16x8*)(lds + PG8_SB(b, h) + boff + n * 2048 + 1024); dst[n].set(f0_, f1_); } } while (0)
; #define PG8_WAIT_V(n) asm volatile("s_waitcnt vmcnt(" #n ")" ::: "memory")
; #define PG8_WAIT_L(n) asm volatile("s_waitcnt lgkmcnt(" #n ")" ::: "memory")
; #define PG8_BAR __builtin_amdgcn_s_barrier()
; #define PG8_SCHED __builtin_amdgcn_sched_barrier(0)
; template <class Epi, class Sched, bool ALIGN_EPI = false, bool SP2 = false>
; __device__ __forceinline__ void gemm_phase(PG8_LAS unsigned char* lds, const Gemm g, const Sched& S, const Epi& E) {
;     ...
;             PG8_LDB(B0, 1, 0); PG8_LDB(B1, 1, 1); PG8_SCHED; PG8_LDA(At, 1, 0); PG8_STAGE(PG8_SA(0, 1), a2 + hstep, voffA);
;             PG8_WAIT_V(8); PG8_WAIT_L(0); PG8_BAR; PG8_MMA(0, 0, At, B0); PG8_MMA(0, 1, At, B1); PG8_BAR; PG8_SCHED;
;             PG8_LDA(At, 1, 1); PG8_STAGE(PG8_SB(1, 0), b3, voffB); PG8_STAGE(PG8_SB(1, 1), b3 + hstepB, voffB); PG8_STAGE(PG8_SA(1, 0), a3, voffA);
	s_add_i32 s33, 0, 0x18000
	s_add_i32 s63, 0, 0x1c000
	v_add_u32_e32 v168, s33, v1
	v_add_u32_e32 v184, s63, v1
	ds_read_b128 v[156:159], v168
	ds_read_b128 v[160:163], v168 offset:1024
	ds_read_b128 v[164:167], v168 offset:2048
	ds_read_b128 v[168:171], v168 offset:3072
	ds_read_b128 v[172:175], v184
	ds_read_b128 v[176:179], v184 offset:1024
	ds_read_b128 v[180:183], v184 offset:2048
	ds_read_b128 v[184:187], v184 offset:3072
	s_add_u32 s0, s34, s12
	s_addc_u32 s1, s35, s13
	s_mov_b32 m0, s42
	v_lshl_add_u64 v[232:233], s[0:1], 0, v[130:131]
	ds_read_b128 v[188:191], v154 offset:32768
	ds_read_b128 v[192:195], v154 offset:33792
	ds_read_b128 v[196:199], v154 offset:34816
	ds_read_b128 v[200:203], v154 offset:35840
	ds_read_b128 v[204:207], v154 offset:36864
	ds_read_b128 v[212:215], v154 offset:37888
	ds_read_b128 v[216:219], v154 offset:38912
	ds_read_b128 v[220:223], v154 offset:39936
	s_mov_b32 m0, s40
	s_nop 0
	global_load_lds_dwordx4 v[228:229], off
	s_mov_b32 m0, s41
	s_nop 0
	global_load_lds_dwordx4 v[230:231], off
	s_mov_b32 m0, s42
	s_nop 0
	global_load_lds_dwordx4 v[232:233], off
	v_lshl_add_u64 v[232:233], s[0:1], 0, v[134:135]
	s_mov_b32 m0, s43
	s_nop 0
	global_load_lds_dwordx4 v[232:233], off
	s_waitcnt vmcnt(8)
	s_waitcnt lgkmcnt(0)
	s_setprio 1
	s_barrier
	s_waitcnt lgkmcnt(0)
	v_mfma_f32_16x16x32_bf16 v[126:129], v[156:159], v[188:191], v[126:129]
	v_mfma_f32_16x16x32_bf16 v[122:125], v[164:167], v[188:191], v[122:125]
	v_mfma_f32_16x16x32_bf16 v[110:113], v[156:159], v[196:199], v[110:113]
	v_mfma_f32_16x16x32_bf16 v[106:109], v[164:167], v[196:199], v[106:109]
	v_mfma_f32_16x16x32_bf16 v[94:97], v[156:159], v[204:207], v[94:97]
	v_mfma_f32_16x16x32_bf16 v[90:93], v[164:167], v[204:207], v[90:93]
	v_mfma_f32_16x16x32_bf16 v[78:81], v[156:159], v[216:219], v[78:81]
	v_mfma_f32_16x16x32_bf16 v[74:77], v[164:167], v[216:219], v[74:77]
	v_mfma_f32_16x16x32_bf16 v[126:129], v[160:163], v[192:195], v[126:129]
	v_mfma_f32_16x16x32_bf16 v[122:125], v[168:171], v[192:195], v[122:125]
	v_mfma_f32_16x16x32_bf16 v[110:113], v[160:163], v[200:203], v[110:113]
	v_mfma_f32_16x16x32_bf16 v[106:109], v[168:171], v[200:203], v[106:109]
	v_mfma_f32_16x16x32_bf16 v[94:97], v[160:163], v[212:215], v[94:97]
	v_mfma_f32_16x16x32_bf16 v[90:93], v[168:171], v[212:215], v[90:93]
	v_mfma_f32_16x16x32_bf16 v[78:81], v[160:163], v[220:223], v[78:81]
	v_mfma_f32_16x16x32_bf16 v[74:77], v[168:171], v[220:223], v[74:77]
	v_mfma_f32_16x16x32_bf16 v[118:121], v[172:175], v[188:191], v[118:121]
	v_mfma_f32_16x16x32_bf16 v[114:117], v[180:183], v[188:191], v[114:117]
	v_mfma_f32_16x16x32_bf16 v[102:105], v[172:175], v[196:199], v[102:105]
	v_mfma_f32_16x16x32_bf16 v[98:101], v[180:183], v[196:199], v[98:101]
	v_mfma_f32_16x16x32_bf16 v[86:89], v[172:175], v[204:207], v[86:89]
	v_mfma_f32_16x16x32_bf16 v[82:85], v[180:183], v[204:207], v[82:85]
	v_mfma_f32_16x16x32_bf16 v[70:73], v[172:175], v[216:219], v[70:73]
	v_mfma_f32_16x16x32_bf16 v[66:69], v[180:183], v[216:219], v[66:69]
	v_mfma_f32_16x16x32_bf16 v[118:121], v[176:179], v[192:195], v[118:121]
	v_mfma_f32_16x16x32_bf16 v[114:117], v[184:187], v[192:195], v[114:117]
	v_mfma_f32_16x16x32_bf16 v[102:105], v[176:179], v[200:203], v[102:105]
	v_mfma_f32_16x16x32_bf16 v[98:101], v[184:187], v[200:203], v[98:101]
	v_mfma_f32_16x16x32_bf16 v[86:89], v[176:179], v[212:215], v[86:89]
	v_mfma_f32_16x16x32_bf16 v[82:85], v[184:187], v[212:215], v[82:85]
	v_mfma_f32_16x16x32_bf16 v[70:73], v[176:179], v[220:223], v[70:73]
	v_mfma_f32_16x16x32_bf16 v[66:69], v[184:187], v[220:223], v[66:69]
	s_setprio 0
	s_barrier
	s_add_i32 s0, s33, s39
	v_lshl_add_u64 v[148:149], v[148:149], 0, s[22:23]
	s_mov_b32 m0, s0
	ds_read_b128 v[188:191], v154 offset:49152
	ds_read_b128 v[192:195], v154 offset:50176
	ds_read_b128 v[196:199], v154 offset:51200
	ds_read_b128 v[200:203], v154 offset:52224
	ds_read_b128 v[204:207], v154 offset:53248
	ds_read_b128 v[212:215], v154 offset:54272
	ds_read_b128 v[216:219], v154 offset:55296
	ds_read_b128 v[220:223], v154 offset:56320
	global_load_lds_dwordx4 v[148:149], off
	v_lshl_add_u64 v[148:149], v[208:209], 0, s[22:23]
	s_add_i32 m0, s0, 0x2000
	s_add_i32 s0, s63, s39
	global_load_lds_dwordx4 v[148:149], off
	v_lshl_add_u64 v[148:149], v[224:225], 0, s[22:23]
	s_mov_b32 m0, s0
	s_nop 0
	global_load_lds_dwordx4 v[148:149], off
	v_lshl_add_u64 v[148:149], v[226:227], 0, s[22:23]
	s_add_i32 m0, s0, 0x2000
	s_nop 0
	global_load_lds_dwordx4 v[148:149], off
	s_cmp_ge_i32 s61, s48
	s_cbranch_scc0 .Lkr4_b
	v_lshl_add_u64 v[148:149], v[228:229], 0, s[22:23]
	s_mov_b32 m0, s46
	s_nop 0
	global_load_lds_dwordx4 v[148:149], off
	v_lshl_add_u64 v[148:149], v[230:231], 0, s[22:23]
	s_mov_b32 m0, s47
	s_nop 0
	global_load_lds_dwordx4 v[148:149], off
; #define PG8_WAIT_V(n) asm volatile("s_waitcnt vmcnt(" #n ")" ::: "memory")
; #define PG8_WAIT_L(n) asm volatile("s_waitcnt lgkmcnt(" #n ")" ::: "memory")
; #define PG8_BAR __builtin_amdgcn_s_barrier()
; #define PG8_SCHED __builtin_amdgcn_sched_barrier(0)
; template <class Epi, class Sched, bool ALIGN_EPI = false, bool SP2 = false>
; __device__ __forceinline__ void gemm_phase(PG8_LAS unsigned char* lds, const Gemm g, const Sched& S, const Epi& E) {
;     ...
;         for (int t = 0; t < nt; t += 2) {
;             if constexpr (Epi::MIDK) { if (t == (nt >> 1)) E.mid(acc, cur, wr, wc, fr, fq); }
;             const bool last = (t == nt - 2);
;             const char* a1 = cA + (size_t)(t + 1) * kstep;
;             const char* a2 = last ? nA : cA + (size_t)(t + 2) * kstep; const char* b2 = last ? nB : cB + (size_t)(t + 2) * kstep;
;             const char* a3 = a2 + kstep; const char* b3 = b2 + kstep;
;     ...
;             PG8_WAIT_V(8); PG8_WAIT_L(0); PG8_BAR; PG8_MMA(1, 0, At, B0); PG8_MMA(1, 1, At, B1); PG8_BAR; PG8_SCHED;
.Lkr4_b:
	s_waitcnt vmcnt(6)
	s_waitcnt lgkmcnt(0)
	s_setprio 1
	s_barrier
	s_waitcnt lgkmcnt(0)
	v_mfma_f32_16x16x32_bf16 v[62:65], v[156:159], v[188:191], v[62:65]
	v_mfma_f32_16x16x32_bf16 v[58:61], v[164:167], v[188:191], v[58:61]
	v_mfma_f32_16x16x32_bf16 v[46:49], v[156:159], v[196:199], v[46:49]
	v_mfma_f32_16x16x32_bf16 v[42:45], v[164:167], v[196:199], v[42:45]
	v_mfma_f32_16x16x32_bf16 v[30:33], v[156:159], v[204:207], v[30:33]
	v_mfma_f32_16x16x32_bf16 v[26:29], v[164:167], v[204:207], v[26:29]
	v_mfma_f32_16x16x32_bf16 v[14:17], v[156:159], v[216:219], v[14:17]
	v_mfma_f32_16x16x32_bf16 v[6:9], v[164:167], v[216:219], v[6:9]
	v_mfma_f32_16x16x32_bf16 v[62:65], v[160:163], v[192:195], v[62:65]
	v_mfma_f32_16x16x32_bf16 v[58:61], v[168:171], v[192:195], v[58:61]
	v_mfma_f32_16x16x32_bf16 v[46:49], v[160:163], v[200:203], v[46:49]
	v_mfma_f32_16x16x32_bf16 v[42:45], v[168:171], v[200:203], v[42:45]
	v_mfma_f32_16x16x32_bf16 v[30:33], v[160:163], v[212:215], v[30:33]
	v_mfma_f32_16x16x32_bf16 v[26:29], v[168:171], v[212:215], v[26:29]
	v_mfma_f32_16x16x32_bf16 v[14:17], v[160:163], v[220:223], v[14:17]
	v_mfma_f32_16x16x32_bf16 v[6:9], v[168:171], v[220:223], v[6:9]
	v_mfma_f32_16x16x32_bf16 v[54:57], v[172:175], v[188:191], v[54:57]
	v_mfma_f32_16x16x32_bf16 v[50:53], v[180:183], v[188:191], v[50:53]
	v_mfma_f32_16x16x32_bf16 v[38:41], v[172:175], v[196:199], v[38:41]
	v_mfma_f32_16x16x32_bf16 v[34:37], v[180:183], v[196:199], v[34:37]
	v_mfma_f32_16x16x32_bf16 v[22:25], v[172:175], v[204:207], v[22:25]
	v_mfma_f32_16x16x32_bf16 v[18:21], v[180:183], v[204:207], v[18:21]
	v_mfma_f32_16x16x32_bf16 v[10:13], v[172:175], v[216:219], v[10:13]
	v_mfma_f32_16x16x32_bf16 v[2:5], v[180:183], v[216:219], v[2:5]
	v_mfma_f32_16x16x32_bf16 v[54:57], v[176:179], v[192:195], v[54:57]
	v_mfma_f32_16x16x32_bf16 v[50:53], v[184:187], v[192:195], v[50:53]
	v_mfma_f32_16x16x32_bf16 v[38:41], v[176:179], v[200:203], v[38:41]
	v_mfma_f32_16x16x32_bf16 v[34:37], v[184:187], v[200:203], v[34:37]
	v_mfma_f32_16x16x32_bf16 v[22:25], v[176:179], v[212:215], v[22:25]
	v_mfma_f32_16x16x32_bf16 v[18:21], v[184:187], v[212:215], v[18:21]
	v_mfma_f32_16x16x32_bf16 v[10:13], v[176:179], v[220:223], v[10:13]
	v_mfma_f32_16x16x32_bf16 v[2:5], v[184:187], v[220:223], v[2:5]
	s_setprio 0
	s_barrier
	s_add_u32 s30, s30, 0x100
	s_addc_u32 s31, s31, 0
	s_add_u32 s58, s58, 0x100
	s_addc_u32 s59, s59, 0
	s_cmp_ge_i32 s61, s48
	s_cselect_b32 s99, 0, 1
	s_mov_b32 s34, s61
	s_cbranch_scc0 .LBB0_1592

; #define PG8_STAGE(bufoff, gbase, voff) do { _Pragma("unroll") for (int _i = 0; _i < 2; ++_i) \
;         __builtin_amdgcn_global_load_lds((const unsigned*)((const char*)(gbase) + (voff)[_i]), (PG8_LAS unsigned*)(lds + (bufoff) + ldsw + _i * 8192), 16, 0, 0); } while (0)
; #define PG8_LDA(dst, b, h) do { _Pragma("unroll") for (int m = 0; m < 4; ++m) { const bf16x8 f0_ = *(const PG8_LAS bf16x8*)(lds + PG8_SA(b, h) + aoff + m * 2048), f1_ = *(const PG8_LAS bf16x8*)(lds + PG8_SA(b, h) + aoff + m * 2048 + 1024); dst[m].set(f0_, f1_); } } while (0)
; #define PG8_LDB(dst, b, h) do { _Pragma("unroll") for (int n = 0; n < 2; ++n) { const bf16x8 f0_ = *(const PG8_LAS bf16x8*)(lds + PG8_SB(b, h) + boff + n * 2048), f1_ = *(const PG8_LAS bf16x8*)(lds + PG8_SB(b, h) + boff + n * 2048 + 1024); dst[n].set(f0_, f1_); } } while (0)
; #define PG8_WAIT_V(n) asm volatile("s_waitcnt vmcnt(" #n ")" ::: "memory")
; #define PG8_WAIT_L(n) asm volatile("s_waitcnt lgkmcnt(" #n ")" ::: "memory")
; #define PG8_BAR __builtin_amdgcn_s_barrier()
; #define PG8_SCHED __builtin_amdgcn_sched_barrier(0)
; template <class Epi, class Sched, bool ALIGN_EPI = false, bool SP2 = false>
; __device__ __forceinline__ void gemm_phase(PG8_LAS unsigned char* lds, const Gemm g, const Sched& S, const Epi& E) {
;     ...
;             PG8_LDB(B0, 0, 0); PG8_LDB(B1, 0, 1); PG8_SCHED; PG8_LDA(At, 0, 0); PG8_STAGE(PG8_SA(1, 1), a1 + hstep, voffA);
;             PG8_WAIT_V(8); PG8_WAIT_L(0); PG8_BAR; PG8_MMA(0, 0, At, B0); PG8_MMA(0, 1, At, B1); PG8_BAR; PG8_SCHED;
;             PG8_LDA(At, 0, 1); PG8_STAGE(PG8_SB(0, 0), b2, voffB); PG8_STAGE(PG8_SB(0, 1), b2 + hstepB, voffB); PG8_STAGE(PG8_SA(0, 0), a2, voffA);
;             PG8_WAIT_V(8); PG8_WAIT_L(0); PG8_BAR; PG8_MMA(1, 0, At, B0); PG8_MMA(1, 1, At, B1); PG8_BAR; PG8_SCHED;
.Lkr5_a:
	v_lshl_add_u64 v[192:193], s[46:47], 0, v[176:177]
	s_add_i32 m0, s10, 0xc000
	ds_read_b128 v[184:187], v199
	ds_read_b128 v[188:191], v199 offset:1024
	ds_read_b128 v[212:215], v199 offset:2048
	ds_read_b128 v[216:219], v199 offset:3072
	ds_read_b128 v[220:223], v199 offset:4096
	ds_read_b128 v[224:227], v199 offset:5120
	ds_read_b128 v[228:231], v199 offset:6144
	ds_read_b128 v[232:235], v199 offset:7168
	global_load_lds_dwordx4 v[192:193], off
	v_lshl_add_u64 v[192:193], s[46:47], 0, v[178:179]
	s_add_i32 m0, s10, 0xe000
	s_nop 0
	global_load_lds_dwordx4 v[192:193], off
	s_waitcnt vmcnt(8)
	s_waitcnt lgkmcnt(0)
	s_setprio 1
	s_barrier
	s_waitcnt lgkmcnt(0)
	v_mfma_scale_f32_16x16x128_f8f6f4 v[158:161], v[18:25], v[184:191], v[158:161], v200, v201 op_sel_hi:[0,0,0]
	v_mfma_scale_f32_16x16x128_f8f6f4 v[154:157], v[26:33], v[184:191], v[154:157], v200, v201 op_sel_hi:[0,0,0]
	v_mfma_scale_f32_16x16x128_f8f6f4 v[142:145], v[18:25], v[212:219], v[142:145], v200, v201 op_sel_hi:[0,0,0]
	v_mfma_scale_f32_16x16x128_f8f6f4 v[138:141], v[26:33], v[212:219], v[138:141], v200, v201 op_sel_hi:[0,0,0]
	v_mfma_scale_f32_16x16x128_f8f6f4 v[126:129], v[18:25], v[220:227], v[126:129], v200, v201 op_sel_hi:[0,0,0]
	v_mfma_scale_f32_16x16x128_f8f6f4 v[122:125], v[26:33], v[220:227], v[122:125], v200, v201 op_sel_hi:[0,0,0]
	v_mfma_scale_f32_16x16x128_f8f6f4 v[110:113], v[18:25], v[228:235], v[110:113], v200, v201 op_sel_hi:[0,0,0]
	v_mfma_scale_f32_16x16x128_f8f6f4 v[106:109], v[26:33], v[228:235], v[106:109], v200, v201 op_sel_hi:[0,0,0]
	v_mfma_scale_f32_16x16x128_f8f6f4 v[150:153], v[2:9], v[184:191], v[150:153], v200, v201 op_sel_hi:[0,0,0]
	v_mfma_scale_f32_16x16x128_f8f6f4 v[146:149], v[10:17], v[184:191], v[146:149], v200, v201 op_sel_hi:[0,0,0]
	v_mfma_scale_f32_16x16x128_f8f6f4 v[134:137], v[2:9], v[212:219], v[134:137], v200, v201 op_sel_hi:[0,0,0]
	v_mfma_scale_f32_16x16x128_f8f6f4 v[130:133], v[10:17], v[212:219], v[130:133], v200, v201 op_sel_hi:[0,0,0]
	v_mfma_scale_f32_16x16x128_f8f6f4 v[118:121], v[2:9], v[220:227], v[118:121], v200, v201 op_sel_hi:[0,0,0]
	v_mfma_scale_f32_16x16x128_f8f6f4 v[114:117], v[10:17], v[220:227], v[114:117], v200, v201 op_sel_hi:[0,0,0]
	v_mfma_scale_f32_16x16x128_f8f6f4 v[102:105], v[2:9], v[228:235], v[102:105], v200, v201 op_sel_hi:[0,0,0]
	v_mfma_scale_f32_16x16x128_f8f6f4 v[98:101], v[10:17], v[228:235], v[98:101], v200, v201 op_sel_hi:[0,0,0]
	s_setprio 0
	s_barrier
	s_add_i32 s0, s73, s9
	v_lshl_add_u64 v[184:185], s[50:51], 0, v[164:165]
	s_mov_b32 m0, s0
	ds_read_b128 v[212:215], v199 offset:16384
	ds_read_b128 v[216:219], v199 offset:17408
	ds_read_b128 v[220:223], v199 offset:18432
	ds_read_b128 v[224:227], v199 offset:19456
	ds_read_b128 v[228:231], v199 offset:20480
	ds_read_b128 v[232:235], v199 offset:21504
	ds_read_b128 v[236:239], v199 offset:22528
	ds_read_b128 v[240:243], v199 offset:23552
	global_load_lds_dwordx4 v[184:185], off
	s_add_i32 m0, s0, 0x2000
	s_add_u32 s0, s50, s14
	v_lshl_add_u64 v[186:187], s[50:51], 0, v[168:169]
	s_addc_u32 s1, s51, s15
	s_add_i32 s33, s74, s9
	global_load_lds_dwordx4 v[186:187], off
	v_lshl_add_u64 v[188:189], s[0:1], 0, v[164:165]
	s_mov_b32 m0, s33
	v_lshl_add_u64 v[190:191], s[0:1], 0, v[168:169]
	global_load_lds_dwordx4 v[188:189], off
	s_add_i32 m0, s33, 0x2000
	v_lshl_add_u64 v[192:193], s[48:49], 0, v[162:163]
	global_load_lds_dwordx4 v[190:191], off
	v_lshl_add_u64 v[194:195], s[48:49], 0, v[166:167]
	s_waitcnt vmcnt(6)
	s_waitcnt lgkmcnt(0)
	s_setprio 1
	s_barrier
	s_waitcnt lgkmcnt(0)
	v_mfma_scale_f32_16x16x128_f8f6f4 v[94:97], v[18:25], v[212:219], v[94:97], v200, v201 op_sel_hi:[0,0,0]
	v_mfma_scale_f32_16x16x128_f8f6f4 v[90:93], v[26:33], v[212:219], v[90:93], v200, v201 op_sel_hi:[0,0,0]
	v_mfma_scale_f32_16x16x128_f8f6f4 v[78:81], v[18:25], v[220:227], v[78:81], v200, v201 op_sel_hi:[0,0,0]
	v_mfma_scale_f32_16x16x128_f8f6f4 v[74:77], v[26:33], v[220:227], v[74:77], v200, v201 op_sel_hi:[0,0,0]
	v_mfma_scale_f32_16x16x128_f8f6f4 v[62:65], v[18:25], v[228:235], v[62:65], v200, v201 op_sel_hi:[0,0,0]
	v_mfma_scale_f32_16x16x128_f8f6f4 v[58:61], v[26:33], v[228:235], v[58:61], v200, v201 op_sel_hi:[0,0,0]
	v_mfma_scale_f32_16x16x128_f8f6f4 v[46:49], v[18:25], v[236:243], v[46:49], v200, v201 op_sel_hi:[0,0,0]
	v_mfma_scale_f32_16x16x128_f8f6f4 v[42:45], v[26:33], v[236:243], v[42:45], v200, v201 op_sel_hi:[0,0,0]
	v_mfma_scale_f32_16x16x128_f8f6f4 v[86:89], v[2:9], v[212:219], v[86:89], v200, v201 op_sel_hi:[0,0,0]
	v_mfma_scale_f32_16x16x128_f8f6f4 v[82:85], v[10:17], v[212:219], v[82:85], v200, v201 op_sel_hi:[0,0,0]
	v_mfma_scale_f32_16x16x128_f8f6f4 v[70:73], v[2:9], v[220:227], v[70:73], v200, v201 op_sel_hi:[0,0,0]
	v_mfma_scale_f32_16x16x128_f8f6f4 v[66:69], v[10:17], v[220:227], v[66:69], v200, v201 op_sel_hi:[0,0,0]
	v_mfma_scale_f32_16x16x128_f8f6f4 v[54:57], v[2:9], v[228:235], v[54:57], v200, v201 op_sel_hi:[0,0,0]
	v_mfma_scale_f32_16x16x128_f8f6f4 v[50:53], v[10:17], v[228:235], v[50:53], v200, v201 op_sel_hi:[0,0,0]
	v_mfma_scale_f32_16x16x128_f8f6f4 v[38:41], v[2:9], v[236:243], v[38:41], v200, v201 op_sel_hi:[0,0,0]
	v_mfma_scale_f32_16x16x128_f8f6f4 v[34:37], v[10:17], v[236:243], v[34:37], v200, v201 op_sel_hi:[0,0,0]
	s_setprio 0
	s_barrier
; #define PG8_STAGE(bufoff, gbase, voff) do { _Pragma("unroll") for (int _i = 0; _i < 2; ++_i) \
;         __builtin_amdgcn_global_load_lds((const unsigned*)((const char*)(gbase) + (voff)[_i]), (PG8_LAS unsigned*)(lds + (bufoff) + ldsw + _i * 8192), 16, 0, 0); } while (0)
; #define PG8_LDA(dst, b, h) do { _Pragma("unroll") for (int m = 0; m < 4; ++m) { const bf16x8 f0_ = *(const PG8_LAS bf16x8*)(lds + PG8_SA(b, h) + aoff + m * 2048), f1_ = *(const PG8_LAS bf16x8*)(lds + PG8_SA(b, h) + aoff + m * 2048 + 1024); dst[m].set(f0_, f1_); } } while (0)
; #define PG8_LDB(dst, b, h) do { _Pragma("unroll") for (int n = 0; n < 2; ++n) { const bf16x8 f0_ = *(const PG8_LAS bf16x8*)(lds + PG8_SB(b, h) + boff + n * 2048), f1_ = *(const PG8_LAS bf16x8*)(lds + PG8_SB(b, h) + boff + n * 2048 + 1024); dst[n].set(f0_, f1_); } } while (0)
; #define PG8_WAIT_V(n) asm volatile("s_waitcnt vmcnt(" #n ")" ::: "memory")
; #define PG8_WAIT_L(n) asm volatile("s_waitcnt lgkmcnt(" #n ")" ::: "memory")
; #define PG8_BAR __builtin_amdgcn_s_barrier()
; #define PG8_SCHED __builtin_amdgcn_sched_barrier(0)
; template <class Epi, class Sched, bool ALIGN_EPI = false, bool SP2 = false>
; __device__ __forceinline__ void gemm_phase(PG8_LAS unsigned char* lds, const Gemm g, const Sched& S, const Epi& E) {
;     ...
;             PG8_LDB(B0, 1, 0); PG8_LDB(B1, 1, 1); PG8_SCHED; PG8_LDA(At, 1, 0); PG8_STAGE(PG8_SA(0, 1), a2 + hstep, voffA);
;             PG8_WAIT_V(8); PG8_WAIT_L(0); PG8_BAR; PG8_MMA(0, 0, At, B0); PG8_MMA(0, 1, At, B1); PG8_BAR; PG8_SCHED;
;             PG8_LDA(At, 1, 1); PG8_STAGE(PG8_SB(1, 0), b3, voffB); PG8_STAGE(PG8_SB(1, 1), b3 + hstepB, voffB); PG8_STAGE(PG8_SA(1, 0), a3, voffA);
;             PG8_WAIT_V(8); PG8_WAIT_L(0); PG8_BAR; PG8_MMA(1, 0, At, B0); PG8_MMA(1, 1, At, B1); PG8_BAR; PG8_SCHED;
	s_add_i32 s33, 0, 0x18000
	s_add_i32 s50, 0, 0x1c000
	v_add_u32_e32 v14, s33, v173
	v_add_u32_e32 v30, s50, v173
	ds_read_b128 v[2:5], v14
	ds_read_b128 v[6:9], v14 offset:1024
	ds_read_b128 v[10:13], v14 offset:2048
	ds_read_b128 v[14:17], v14 offset:3072
	ds_read_b128 v[18:21], v30
	ds_read_b128 v[22:25], v30 offset:1024
	ds_read_b128 v[26:29], v30 offset:2048
	ds_read_b128 v[30:33], v30 offset:3072
	s_add_u32 s0, s48, s12
	s_addc_u32 s1, s49, s13
	s_mov_b32 m0, s52
	v_lshl_add_u64 v[204:205], s[0:1], 0, v[162:163]
	ds_read_b128 v[212:215], v199 offset:32768
	ds_read_b128 v[216:219], v199 offset:33792
	ds_read_b128 v[220:223], v199 offset:34816
	ds_read_b128 v[224:227], v199 offset:35840
	ds_read_b128 v[228:231], v199 offset:36864
	ds_read_b128 v[232:235], v199 offset:37888
	ds_read_b128 v[236:239], v199 offset:38912
	ds_read_b128 v[240:243], v199 offset:39936
	s_mov_b32 m0, s10
	s_nop 0
	global_load_lds_dwordx4 v[192:193], off
	s_mov_b32 m0, s11
	s_nop 0
	global_load_lds_dwordx4 v[194:195], off
	s_mov_b32 m0, s52
	s_nop 0
	global_load_lds_dwordx4 v[204:205], off
	v_lshl_add_u64 v[204:205], s[0:1], 0, v[166:167]
	s_mov_b32 m0, s53
	s_nop 0
	global_load_lds_dwordx4 v[204:205], off
	s_waitcnt vmcnt(8)
	s_waitcnt lgkmcnt(0)
	s_setprio 1
	s_barrier
	s_waitcnt lgkmcnt(0)
	v_mfma_scale_f32_16x16x128_f8f6f4 v[158:161], v[2:9], v[212:219], v[158:161], v200, v201 op_sel_hi:[0,0,0]
	v_mfma_scale_f32_16x16x128_f8f6f4 v[154:157], v[10:17], v[212:219], v[154:157], v200, v201 op_sel_hi:[0,0,0]
	v_mfma_scale_f32_16x16x128_f8f6f4 v[142:145], v[2:9], v[220:227], v[142:145], v200, v201 op_sel_hi:[0,0,0]
	v_mfma_scale_f32_16x16x128_f8f6f4 v[138:141], v[10:17], v[220:227], v[138:141], v200, v201 op_sel_hi:[0,0,0]
	v_mfma_scale_f32_16x16x128_f8f6f4 v[126:129], v[2:9], v[228:235], v[126:129], v200, v201 op_sel_hi:[0,0,0]
	v_mfma_scale_f32_16x16x128_f8f6f4 v[122:125], v[10:17], v[228:235], v[122:125], v200, v201 op_sel_hi:[0,0,0]
	v_mfma_scale_f32_16x16x128_f8f6f4 v[110:113], v[2:9], v[236:243], v[110:113], v200, v201 op_sel_hi:[0,0,0]
	v_mfma_scale_f32_16x16x128_f8f6f4 v[106:109], v[10:17], v[236:243], v[106:109], v200, v201 op_sel_hi:[0,0,0]
	v_mfma_scale_f32_16x16x128_f8f6f4 v[150:153], v[18:25], v[212:219], v[150:153], v200, v201 op_sel_hi:[0,0,0]
	v_mfma_scale_f32_16x16x128_f8f6f4 v[146:149], v[26:33], v[212:219], v[146:149], v200, v201 op_sel_hi:[0,0,0]
	v_mfma_scale_f32_16x16x128_f8f6f4 v[134:137], v[18:25], v[220:227], v[134:137], v200, v201 op_sel_hi:[0,0,0]
	v_mfma_scale_f32_16x16x128_f8f6f4 v[130:133], v[26:33], v[220:227], v[130:133], v200, v201 op_sel_hi:[0,0,0]
	v_mfma_scale_f32_16x16x128_f8f6f4 v[118:121], v[18:25], v[228:235], v[118:121], v200, v201 op_sel_hi:[0,0,0]
	v_mfma_scale_f32_16x16x128_f8f6f4 v[114:117], v[26:33], v[228:235], v[114:117], v200, v201 op_sel_hi:[0,0,0]
	v_mfma_scale_f32_16x16x128_f8f6f4 v[102:105], v[18:25], v[236:243], v[102:105], v200, v201 op_sel_hi:[0,0,0]
	v_mfma_scale_f32_16x16x128_f8f6f4 v[98:101], v[26:33], v[236:243], v[98:101], v200, v201 op_sel_hi:[0,0,0]
	s_setprio 0
	s_barrier
	s_add_i32 s0, s33, s9
	v_lshl_add_u64 v[184:185], v[184:185], 0, s[28:29]
	s_mov_b32 m0, s0
	ds_read_b128 v[212:215], v199 offset:49152
	ds_read_b128 v[216:219], v199 offset:50176
	ds_read_b128 v[220:223], v199 offset:51200
	ds_read_b128 v[224:227], v199 offset:52224
	ds_read_b128 v[228:231], v199 offset:53248
	ds_read_b128 v[232:235], v199 offset:54272
	ds_read_b128 v[236:239], v199 offset:55296
	ds_read_b128 v[240:243], v199 offset:56320
	global_load_lds_dwordx4 v[184:185], off
	v_lshl_add_u64 v[184:185], v[186:187], 0, s[28:29]
	s_add_i32 m0, s0, 0x2000
	s_add_i32 s0, s50, s9
	global_load_lds_dwordx4 v[184:185], off
	v_lshl_add_u64 v[184:185], v[188:189], 0, s[28:29]
	s_mov_b32 m0, s0
	s_nop 0
	global_load_lds_dwordx4 v[184:185], off
	v_lshl_add_u64 v[184:185], v[190:191], 0, s[28:29]
	s_add_i32 m0, s0, 0x2000
	s_nop 0
	global_load_lds_dwordx4 v[184:185], off
	s_cmp_ge_i32 s82, s58
	s_cbranch_scc0 .Lkr5_b
	v_lshl_add_u64 v[184:185], v[192:193], 0, s[28:29]
	s_mov_b32 m0, s56
	s_nop 0
	global_load_lds_dwordx4 v[184:185], off
	v_lshl_add_u64 v[184:185], v[194:195], 0, s[28:29]
	s_mov_b32 m0, s57
	s_nop 0
	global_load_lds_dwordx4 v[184:185], off
.Lkr5_b:
	s_waitcnt vmcnt(6)
	s_waitcnt lgkmcnt(0)
	s_setprio 1
	s_barrier
	s_waitcnt lgkmcnt(0)
	v_mfma_scale_f32_16x16x128_f8f6f4 v[94:97], v[2:9], v[212:219], v[94:97], v200, v201 op_sel_hi:[0,0,0]
	v_mfma_scale_f32_16x16x128_f8f6f4 v[90:93], v[10:17], v[212:219], v[90:93], v200, v201 op_sel_hi:[0,0,0]
	v_mfma_scale_f32_16x16x128_f8f6f4 v[78:81], v[2:9], v[220:227], v[78:81], v200, v201 op_sel_hi:[0,0,0]
	v_mfma_scale_f32_16x16x128_f8f6f4 v[74:77], v[10:17], v[220:227], v[74:77], v200, v201 op_sel_hi:[0,0,0]
	v_mfma_scale_f32_16x16x128_f8f6f4 v[62:65], v[2:9], v[228:235], v[62:65], v200, v201 op_sel_hi:[0,0,0]
	v_mfma_scale_f32_16x16x128_f8f6f4 v[58:61], v[10:17], v[228:235], v[58:61], v200, v201 op_sel_hi:[0,0,0]
	v_mfma_scale_f32_16x16x128_f8f6f4 v[46:49], v[2:9], v[236:243], v[46:49], v200, v201 op_sel_hi:[0,0,0]
	v_mfma_scale_f32_16x16x128_f8f6f4 v[42:45], v[10:17], v[236:243], v[42:45], v200, v201 op_sel_hi:[0,0,0]
	v_mfma_scale_f32_16x16x128_f8f6f4 v[86:89], v[18:25], v[212:219], v[86:89], v200, v201 op_sel_hi:[0,0,0]
	v_mfma_scale_f32_16x16x128_f8f6f4 v[82:85], v[26:33], v[212:219], v[82:85], v200, v201 op_sel_hi:[0,0,0]
	v_mfma_scale_f32_16x16x128_f8f6f4 v[70:73], v[18:25], v[220:227], v[70:73], v200, v201 op_sel_hi:[0,0,0]
	v_mfma_scale_f32_16x16x128_f8f6f4 v[66:69], v[26:33], v[220:227], v[66:69], v200, v201 op_sel_hi:[0,0,0]
	v_mfma_scale_f32_16x16x128_f8f6f4 v[54:57], v[18:25], v[228:235], v[54:57], v200, v201 op_sel_hi:[0,0,0]
	v_mfma_scale_f32_16x16x128_f8f6f4 v[50:53], v[26:33], v[228:235], v[50:53], v200, v201 op_sel_hi:[0,0,0]
	v_mfma_scale_f32_16x16x128_f8f6f4 v[38:41], v[18:25], v[236:243], v[38:41], v200, v201 op_sel_hi:[0,0,0]
	v_mfma_scale_f32_16x16x128_f8f6f4 v[34:37], v[26:33], v[236:243], v[34:37], v200, v201 op_sel_hi:[0,0,0]
	s_setprio 0
	s_barrier
	s_add_u32 s46, s46, 0x100
	s_addc_u32 s47, s47, 0
	s_add_u32 s80, s80, 0x100
	s_addc_u32 s81, s81, 0
	s_cmp_ge_i32 s82, s58
	s_cselect_b32 s99, 0, 1
	s_mov_b32 s48, s82
	s_cbranch_scc0 .LBB0_1625

; #define PG8_STAGE(bufoff, gbase, voff) do { _Pragma("unroll") for (int _i = 0; _i < 2; ++_i) \
;         __builtin_amdgcn_global_load_lds((const unsigned*)((const char*)(gbase) + (voff)[_i]), (PG8_LAS unsigned*)(lds + (bufoff) + ldsw + _i * 8192), 16, 0, 0); } while (0)
; #define PG8_LDA(dst, b, h) do { _Pragma("unroll") for (int m = 0; m < 4; ++m) { const bf16x8 f0_ = *(const PG8_LAS bf16x8*)(lds + PG8_SA(b, h) + aoff + m * 2048), f1_ = *(const PG8_LAS bf16x8*)(lds + PG8_SA(b, h) + aoff + m * 2048 + 1024); dst[m].set(f0_, f1_); } } while (0)
; #define PG8_LDB(dst, b, h) do { _Pragma("unroll") for (int n = 0; n < 2; ++n) { const bf16x8 f0_ = *(const PG8_LAS bf16x8*)(lds + PG8_SB(b, h) + boff + n * 2048), f1_ = *(const PG8_LAS bf16x8*)(lds + PG8_SB(b, h) + boff + n * 2048 + 1024); dst[n].set(f0_, f1_); } } while (0)
; #define PG8_WAIT_V(n) asm volatile("s_waitcnt vmcnt(" #n ")" ::: "memory")
; #define PG8_WAIT_L(n) asm volatile("s_waitcnt lgkmcnt(" #n ")" ::: "memory")
; #define PG8_BAR __builtin_amdgcn_s_barrier()
; #define PG8_SCHED __builtin_amdgcn_sched_barrier(0)
; template <class Epi, class Sched, bool ALIGN_EPI = false, bool SP2 = false>
; __device__ __forceinline__ void gemm_phase(PG8_LAS unsigned char* lds, const Gemm g, const Sched& S, const Epi& E) {
;     ...
;             PG8_LDB(B0, 0, 0); PG8_LDB(B1, 0, 1); PG8_SCHED; PG8_LDA(At, 0, 0); PG8_STAGE(PG8_SA(1, 1), a1 + hstep, voffA);
;             PG8_WAIT_V(8); PG8_WAIT_L(0); PG8_BAR; PG8_MMA(0, 0, At, B0); PG8_MMA(0, 1, At, B1); PG8_BAR; PG8_SCHED;
;             PG8_LDA(At, 0, 1); PG8_STAGE(PG8_SB(0, 0), b2, voffB); PG8_STAGE(PG8_SB(0, 1), b2 + hstepB, voffB); PG8_STAGE(PG8_SA(0, 0), a2, voffA);
;             PG8_WAIT_V(8); PG8_WAIT_L(0); PG8_BAR; PG8_MMA(1, 0, At, B0); PG8_MMA(1, 1, At, B1); PG8_BAR; PG8_SCHED;
.Lkr6_a:
	v_lshl_add_u64 v[206:207], s[2:3], 0, v[198:199]
	s_add_i32 m0, s71, 0xc000
	ds_read_b128 v[152:155], v217
	ds_read_b128 v[156:159], v217 offset:1024
	ds_read_b128 v[168:171], v217 offset:2048
	ds_read_b128 v[172:175], v217 offset:3072
	ds_read_b128 v[176:179], v217 offset:4096
	ds_read_b128 v[180:183], v217 offset:5120
	ds_read_b128 v[226:229], v217 offset:6144
	ds_read_b128 v[230:233], v217 offset:7168
	global_load_lds_dwordx4 v[206:207], off
	v_lshl_add_u64 v[206:207], s[2:3], 0, v[200:201]
	s_add_i32 m0, s71, 0xe000
	s_nop 0
	global_load_lds_dwordx4 v[206:207], off
	s_waitcnt vmcnt(8)
	s_waitcnt lgkmcnt(0)
	s_setprio 1
	s_barrier
	s_waitcnt lgkmcnt(0)
	v_mfma_scale_f32_16x16x128_f8f6f4 v[164:167], v[16:23], v[152:159], v[164:167], v218, v219 op_sel_hi:[0,0,0]
	v_mfma_scale_f32_16x16x128_f8f6f4 v[160:163], v[24:31], v[152:159], v[160:163], v218, v219 op_sel_hi:[0,0,0]
	v_mfma_scale_f32_16x16x128_f8f6f4 v[140:143], v[16:23], v[168:175], v[140:143], v218, v219 op_sel_hi:[0,0,0]
	v_mfma_scale_f32_16x16x128_f8f6f4 v[136:139], v[24:31], v[168:175], v[136:139], v218, v219 op_sel_hi:[0,0,0]
	v_mfma_scale_f32_16x16x128_f8f6f4 v[108:111], v[16:23], v[176:183], v[108:111], v218, v219 op_sel_hi:[0,0,0]
	v_mfma_scale_f32_16x16x128_f8f6f4 v[104:107], v[24:31], v[176:183], v[104:107], v218, v219 op_sel_hi:[0,0,0]
	v_mfma_scale_f32_16x16x128_f8f6f4 v[116:119], v[16:23], v[226:233], v[116:119], v218, v219 op_sel_hi:[0,0,0]
	v_mfma_scale_f32_16x16x128_f8f6f4 v[112:115], v[24:31], v[226:233], v[112:115], v218, v219 op_sel_hi:[0,0,0]
	v_mfma_scale_f32_16x16x128_f8f6f4 v[148:151], v[0:7], v[152:159], v[148:151], v218, v219 op_sel_hi:[0,0,0]
	v_mfma_scale_f32_16x16x128_f8f6f4 v[144:147], v[8:15], v[152:159], v[144:147], v218, v219 op_sel_hi:[0,0,0]
	v_mfma_scale_f32_16x16x128_f8f6f4 v[132:135], v[0:7], v[168:175], v[132:135], v218, v219 op_sel_hi:[0,0,0]
	v_mfma_scale_f32_16x16x128_f8f6f4 v[128:131], v[8:15], v[168:175], v[128:131], v218, v219 op_sel_hi:[0,0,0]
	v_mfma_scale_f32_16x16x128_f8f6f4 v[124:127], v[0:7], v[176:183], v[124:127], v218, v219 op_sel_hi:[0,0,0]
	v_mfma_scale_f32_16x16x128_f8f6f4 v[120:123], v[8:15], v[176:183], v[120:123], v218, v219 op_sel_hi:[0,0,0]
	v_mfma_scale_f32_16x16x128_f8f6f4 v[100:103], v[0:7], v[226:233], v[100:103], v218, v219 op_sel_hi:[0,0,0]
	v_mfma_scale_f32_16x16x128_f8f6f4 v[96:99], v[8:15], v[226:233], v[96:99], v218, v219 op_sel_hi:[0,0,0]
	s_setprio 0
	s_barrier
	s_add_i32 s0, s67, s45
	v_lshl_add_u64 v[152:153], s[80:81], 0, v[186:187]
	s_mov_b32 m0, s0
	ds_read_b128 v[172:175], v217 offset:16384
	ds_read_b128 v[176:179], v217 offset:17408
	ds_read_b128 v[226:229], v217 offset:18432
	ds_read_b128 v[230:233], v217 offset:19456
	ds_read_b128 v[234:237], v217 offset:20480
	ds_read_b128 v[238:241], v217 offset:21504
	ds_read_b128 v[242:245], v217 offset:22528
	ds_read_b128 v[246:249], v217 offset:23552
	global_load_lds_dwordx4 v[152:153], off
	s_add_i32 m0, s0, 0x2000
	s_add_u32 s0, s80, s20
	v_lshl_add_u64 v[154:155], s[80:81], 0, v[190:191]
	s_addc_u32 s1, s81, s21
	s_add_i32 s33, s10, s45
	global_load_lds_dwordx4 v[154:155], off
	v_lshl_add_u64 v[156:157], s[0:1], 0, v[186:187]
	s_mov_b32 m0, s33
	v_lshl_add_u64 v[158:159], s[0:1], 0, v[190:191]
	global_load_lds_dwordx4 v[156:157], off
	s_add_i32 m0, s33, 0x2000
	v_lshl_add_u64 v[168:169], s[78:79], 0, v[184:185]
	global_load_lds_dwordx4 v[158:159], off
	v_lshl_add_u64 v[170:171], s[78:79], 0, v[188:189]
	s_waitcnt vmcnt(6)
	s_waitcnt lgkmcnt(0)
	s_setprio 1
	s_barrier
	s_waitcnt lgkmcnt(0)
	v_mfma_scale_f32_16x16x128_f8f6f4 v[92:95], v[16:23], v[172:179], v[92:95], v218, v219 op_sel_hi:[0,0,0]
	v_mfma_scale_f32_16x16x128_f8f6f4 v[88:91], v[24:31], v[172:179], v[88:91], v218, v219 op_sel_hi:[0,0,0]
	v_mfma_scale_f32_16x16x128_f8f6f4 v[76:79], v[16:23], v[226:233], v[76:79], v218, v219 op_sel_hi:[0,0,0]
	v_mfma_scale_f32_16x16x128_f8f6f4 v[72:75], v[24:31], v[226:233], v[72:75], v218, v219 op_sel_hi:[0,0,0]
	v_mfma_scale_f32_16x16x128_f8f6f4 v[60:63], v[16:23], v[234:241], v[60:63], v218, v219 op_sel_hi:[0,0,0]
	v_mfma_scale_f32_16x16x128_f8f6f4 v[56:59], v[24:31], v[234:241], v[56:59], v218, v219 op_sel_hi:[0,0,0]
	v_mfma_scale_f32_16x16x128_f8f6f4 v[44:47], v[16:23], v[242:249], v[44:47], v218, v219 op_sel_hi:[0,0,0]
	v_mfma_scale_f32_16x16x128_f8f6f4 v[40:43], v[24:31], v[242:249], v[40:43], v218, v219 op_sel_hi:[0,0,0]
	v_mfma_scale_f32_16x16x128_f8f6f4 v[84:87], v[0:7], v[172:179], v[84:87], v218, v219 op_sel_hi:[0,0,0]
	v_mfma_scale_f32_16x16x128_f8f6f4 v[80:83], v[8:15], v[172:179], v[80:83], v218, v219 op_sel_hi:[0,0,0]
	v_mfma_scale_f32_16x16x128_f8f6f4 v[68:71], v[0:7], v[226:233], v[68:71], v218, v219 op_sel_hi:[0,0,0]
	v_mfma_scale_f32_16x16x128_f8f6f4 v[64:67], v[8:15], v[226:233], v[64:67], v218, v219 op_sel_hi:[0,0,0]
	v_mfma_scale_f32_16x16x128_f8f6f4 v[52:55], v[0:7], v[234:241], v[52:55], v218, v219 op_sel_hi:[0,0,0]
	v_mfma_scale_f32_16x16x128_f8f6f4 v[48:51], v[8:15], v[234:241], v[48:51], v218, v219 op_sel_hi:[0,0,0]
	v_mfma_scale_f32_16x16x128_f8f6f4 v[36:39], v[0:7], v[242:249], v[36:39], v218, v219 op_sel_hi:[0,0,0]
	v_mfma_scale_f32_16x16x128_f8f6f4 v[32:35], v[8:15], v[242:249], v[32:35], v218, v219 op_sel_hi:[0,0,0]
	s_setprio 0
	s_barrier
; #define PG8_STAGE(bufoff, gbase, voff) do { _Pragma("unroll") for (int _i = 0; _i < 2; ++_i) \
;         __builtin_amdgcn_global_load_lds((const unsigned*)((const char*)(gbase) + (voff)[_i]), (PG8_LAS unsigned*)(lds + (bufoff) + ldsw + _i * 8192), 16, 0, 0); } while (0)
; #define PG8_LDA(dst, b, h) do { _Pragma("unroll") for (int m = 0; m < 4; ++m) { const bf16x8 f0_ = *(const PG8_LAS bf16x8*)(lds + PG8_SA(b, h) + aoff + m * 2048), f1_ = *(const PG8_LAS bf16x8*)(lds + PG8_SA(b, h) + aoff + m * 2048 + 1024); dst[m].set(f0_, f1_); } } while (0)
; #define PG8_LDB(dst, b, h) do { _Pragma("unroll") for (int n = 0; n < 2; ++n) { const bf16x8 f0_ = *(const PG8_LAS bf16x8*)(lds + PG8_SB(b, h) + boff + n * 2048), f1_ = *(const PG8_LAS bf16x8*)(lds + PG8_SB(b, h) + boff + n * 2048 + 1024); dst[n].set(f0_, f1_); } } while (0)
; #define PG8_WAIT_V(n) asm volatile("s_waitcnt vmcnt(" #n ")" ::: "memory")
; #define PG8_WAIT_L(n) asm volatile("s_waitcnt lgkmcnt(" #n ")" ::: "memory")
; #define PG8_BAR __builtin_amdgcn_s_barrier()
; #define PG8_SCHED __builtin_amdgcn_sched_barrier(0)
; template <class Epi, class Sched, bool ALIGN_EPI = false, bool SP2 = false>
; __device__ __forceinline__ void gemm_phase(PG8_LAS unsigned char* lds, const Gemm g, const Sched& S, const Epi& E) {
;     ...
;             PG8_LDB(B0, 1, 0); PG8_LDB(B1, 1, 1); PG8_SCHED; PG8_LDA(At, 1, 0); PG8_STAGE(PG8_SA(0, 1), a2 + hstep, voffA);
;             PG8_WAIT_V(8); PG8_WAIT_L(0); PG8_BAR; PG8_MMA(0, 0, At, B0); PG8_MMA(0, 1, At, B1); PG8_BAR; PG8_SCHED;
;             PG8_LDA(At, 1, 1); PG8_STAGE(PG8_SB(1, 0), b3, voffB); PG8_STAGE(PG8_SB(1, 1), b3 + hstepB, voffB); PG8_STAGE(PG8_SA(1, 0), a3, voffA);
;             PG8_WAIT_V(8); PG8_WAIT_L(0); PG8_BAR; PG8_MMA(1, 0, At, B0); PG8_MMA(1, 1, At, B1); PG8_BAR; PG8_SCHED;
	s_add_i32 s33, 0, 0x18000
	s_add_i32 s80, 0, 0x1c000
	v_add_u32_e32 v12, s33, v211
	v_add_u32_e32 v28, s80, v211
	ds_read_b128 v[0:3], v12
	ds_read_b128 v[4:7], v12 offset:1024
	ds_read_b128 v[8:11], v12 offset:2048
	ds_read_b128 v[12:15], v12 offset:3072
	ds_read_b128 v[16:19], v28
	ds_read_b128 v[20:23], v28 offset:1024
	ds_read_b128 v[24:27], v28 offset:2048
	ds_read_b128 v[28:31], v28 offset:3072
	s_add_u32 s0, s78, s18
	s_addc_u32 s1, s79, s19
	s_mov_b32 m0, s86
	v_lshl_add_u64 v[180:181], s[0:1], 0, v[184:185]
	ds_read_b128 v[172:175], v217 offset:32768
	ds_read_b128 v[176:179], v217 offset:33792
	ds_read_b128 v[226:229], v217 offset:34816
	ds_read_b128 v[230:233], v217 offset:35840
	ds_read_b128 v[234:237], v217 offset:36864
	ds_read_b128 v[238:241], v217 offset:37888
	ds_read_b128 v[242:245], v217 offset:38912
	ds_read_b128 v[246:249], v217 offset:39936
	s_mov_b32 m0, s71
	s_nop 0
	global_load_lds_dwordx4 v[168:169], off
	s_mov_b32 m0, s73
	s_nop 0
	global_load_lds_dwordx4 v[170:171], off
	s_mov_b32 m0, s86
	s_nop 0
	global_load_lds_dwordx4 v[180:181], off
	v_lshl_add_u64 v[180:181], s[0:1], 0, v[188:189]
	s_mov_b32 m0, s87
	s_nop 0
	global_load_lds_dwordx4 v[180:181], off
	s_waitcnt vmcnt(8)
	s_waitcnt lgkmcnt(0)
	s_setprio 1
	s_barrier
	s_waitcnt lgkmcnt(0)
	v_mfma_scale_f32_16x16x128_f8f6f4 v[164:167], v[0:7], v[172:179], v[164:167], v218, v219 op_sel_hi:[0,0,0]
	v_mfma_scale_f32_16x16x128_f8f6f4 v[160:163], v[8:15], v[172:179], v[160:163], v218, v219 op_sel_hi:[0,0,0]
	v_mfma_scale_f32_16x16x128_f8f6f4 v[140:143], v[0:7], v[226:233], v[140:143], v218, v219 op_sel_hi:[0,0,0]
	v_mfma_scale_f32_16x16x128_f8f6f4 v[136:139], v[8:15], v[226:233], v[136:139], v218, v219 op_sel_hi:[0,0,0]
	v_mfma_scale_f32_16x16x128_f8f6f4 v[108:111], v[0:7], v[234:241], v[108:111], v218, v219 op_sel_hi:[0,0,0]
	v_mfma_scale_f32_16x16x128_f8f6f4 v[104:107], v[8:15], v[234:241], v[104:107], v218, v219 op_sel_hi:[0,0,0]
	v_mfma_scale_f32_16x16x128_f8f6f4 v[116:119], v[0:7], v[242:249], v[116:119], v218, v219 op_sel_hi:[0,0,0]
	v_mfma_scale_f32_16x16x128_f8f6f4 v[112:115], v[8:15], v[242:249], v[112:115], v218, v219 op_sel_hi:[0,0,0]
	v_mfma_scale_f32_16x16x128_f8f6f4 v[148:151], v[16:23], v[172:179], v[148:151], v218, v219 op_sel_hi:[0,0,0]
	v_mfma_scale_f32_16x16x128_f8f6f4 v[144:147], v[24:31], v[172:179], v[144:147], v218, v219 op_sel_hi:[0,0,0]
	v_mfma_scale_f32_16x16x128_f8f6f4 v[132:135], v[16:23], v[226:233], v[132:135], v218, v219 op_sel_hi:[0,0,0]
	v_mfma_scale_f32_16x16x128_f8f6f4 v[128:131], v[24:31], v[226:233], v[128:131], v218, v219 op_sel_hi:[0,0,0]
	v_mfma_scale_f32_16x16x128_f8f6f4 v[124:127], v[16:23], v[234:241], v[124:127], v218, v219 op_sel_hi:[0,0,0]
	v_mfma_scale_f32_16x16x128_f8f6f4 v[120:123], v[24:31], v[234:241], v[120:123], v218, v219 op_sel_hi:[0,0,0]
	v_mfma_scale_f32_16x16x128_f8f6f4 v[100:103], v[16:23], v[242:249], v[100:103], v218, v219 op_sel_hi:[0,0,0]
	v_mfma_scale_f32_16x16x128_f8f6f4 v[96:99], v[24:31], v[242:249], v[96:99], v218, v219 op_sel_hi:[0,0,0]
	s_setprio 0
	s_barrier
	s_add_i32 s0, s33, s45
	v_lshl_add_u64 v[152:153], v[152:153], 0, s[36:37]
	s_mov_b32 m0, s0
	ds_read_b128 v[172:175], v217 offset:49152
	ds_read_b128 v[176:179], v217 offset:50176
	ds_read_b128 v[226:229], v217 offset:51200
	ds_read_b128 v[230:233], v217 offset:52224
	ds_read_b128 v[234:237], v217 offset:53248
	ds_read_b128 v[238:241], v217 offset:54272
	ds_read_b128 v[242:245], v217 offset:55296
	ds_read_b128 v[246:249], v217 offset:56320
	global_load_lds_dwordx4 v[152:153], off
	v_lshl_add_u64 v[152:153], v[154:155], 0, s[36:37]
	s_add_i32 m0, s0, 0x2000
	s_add_i32 s0, s80, s45
	global_load_lds_dwordx4 v[152:153], off
	v_lshl_add_u64 v[152:153], v[156:157], 0, s[36:37]
	s_mov_b32 m0, s0
	s_nop 0
	global_load_lds_dwordx4 v[152:153], off
	v_lshl_add_u64 v[152:153], v[158:159], 0, s[36:37]
	s_add_i32 m0, s0, 0x2000
	s_nop 0
	global_load_lds_dwordx4 v[152:153], off
	s_cmp_ge_i32 s83, s91
	s_cbranch_scc0 .Lkr6_b
	v_lshl_add_u64 v[152:153], v[168:169], 0, s[36:37]
	s_mov_b32 m0, s93
	s_nop 0
	global_load_lds_dwordx4 v[152:153], off
	v_lshl_add_u64 v[152:153], v[170:171], 0, s[36:37]
	s_mov_b32 m0, s94
	s_nop 0
	global_load_lds_dwordx4 v[152:153], off
.Lkr6_b:
	s_waitcnt vmcnt(6)
	s_waitcnt lgkmcnt(0)
	s_setprio 1
	s_barrier
	s_waitcnt lgkmcnt(0)
	v_mfma_scale_f32_16x16x128_f8f6f4 v[92:95], v[0:7], v[172:179], v[92:95], v218, v219 op_sel_hi:[0,0,0]
	v_mfma_scale_f32_16x16x128_f8f6f4 v[88:91], v[8:15], v[172:179], v[88:91], v218, v219 op_sel_hi:[0,0,0]
	v_mfma_scale_f32_16x16x128_f8f6f4 v[76:79], v[0:7], v[226:233], v[76:79], v218, v219 op_sel_hi:[0,0,0]
	v_mfma_scale_f32_16x16x128_f8f6f4 v[72:75], v[8:15], v[226:233], v[72:75], v218, v219 op_sel_hi:[0,0,0]
	v_mfma_scale_f32_16x16x128_f8f6f4 v[60:63], v[0:7], v[234:241], v[60:63], v218, v219 op_sel_hi:[0,0,0]
	v_mfma_scale_f32_16x16x128_f8f6f4 v[56:59], v[8:15], v[234:241], v[56:59], v218, v219 op_sel_hi:[0,0,0]
	v_mfma_scale_f32_16x16x128_f8f6f4 v[44:47], v[0:7], v[242:249], v[44:47], v218, v219 op_sel_hi:[0,0,0]
	v_mfma_scale_f32_16x16x128_f8f6f4 v[40:43], v[8:15], v[242:249], v[40:43], v218, v219 op_sel_hi:[0,0,0]
	v_mfma_scale_f32_16x16x128_f8f6f4 v[84:87], v[16:23], v[172:179], v[84:87], v218, v219 op_sel_hi:[0,0,0]
	v_mfma_scale_f32_16x16x128_f8f6f4 v[80:83], v[24:31], v[172:179], v[80:83], v218, v219 op_sel_hi:[0,0,0]
	v_mfma_scale_f32_16x16x128_f8f6f4 v[68:71], v[16:23], v[226:233], v[68:71], v218, v219 op_sel_hi:[0,0,0]
	v_mfma_scale_f32_16x16x128_f8f6f4 v[64:67], v[24:31], v[226:233], v[64:67], v218, v219 op_sel_hi:[0,0,0]
	v_mfma_scale_f32_16x16x128_f8f6f4 v[52:55], v[16:23], v[234:241], v[52:55], v218, v219 op_sel_hi:[0,0,0]
	v_mfma_scale_f32_16x16x128_f8f6f4 v[48:51], v[24:31], v[234:241], v[48:51], v218, v219 op_sel_hi:[0,0,0]
	v_mfma_scale_f32_16x16x128_f8f6f4 v[36:39], v[16:23], v[242:249], v[36:39], v218, v219 op_sel_hi:[0,0,0]
	v_mfma_scale_f32_16x16x128_f8f6f4 v[32:35], v[24:31], v[242:249], v[32:35], v218, v219 op_sel_hi:[0,0,0]
	s_setprio 0
	s_barrier
	s_add_u32 s2, s2, 0x100
	s_addc_u32 s3, s3, 0
	s_add_u32 s57, s57, 0x100
	s_addc_u32 s82, s82, 0
	s_cmp_ge_i32 s83, s91
	s_cselect_b32 s99, 0, 1
	s_mov_b32 s78, s83
	s_cbranch_scc0 .LBB0_1658
